# speedup vs baseline: 1.0116x; 1.0116x over previous
_Z7gemm128ILi2ELi128EEv8GemmArgs:
	s_cmp_ge_u32 s2, 0x100
	s_cbranch_scc1 .Lup_exit
	s_load_dwordx4 s[4:7], s[0:1], 0x0
	s_load_dwordx2 s[8:9], s[0:1], 0x20
	s_load_dwordx2 s[10:11], s[0:1], 0x48
	s_and_b32 s12, s2, 7
	s_lshr_b32 s13, s2, 3
	s_lshl_b32 s12, s12, 5
	s_add_u32 s12, s12, s13
	s_and_b32 s13, s12, 3
	s_lshr_b32 s12, s12, 2
	s_lshl_b32 s12, s12, 7
	s_lshl_b32 s13, s13, 8
	s_add_u32 s13, s13, 0x800
	s_mov_b32 s24, 0xc0135761
	v_lshrrev_b32_e32 v1, 6, v0
	v_and_b32_e32 v24, 7, v0
	v_bfe_u32 v25, v0, 4, 3
	v_xor_b32_e32 v24, v24, v25
	v_readfirstlane_b32 s14, v1
	v_lshrrev_b32_e32 v25, 3, v0
	v_mul_u32_u24_e32 v25, 0x600, v25
	v_lshl_add_u32 v2, v24, 4, v25
	s_mov_b32 s22, 0xc000
	v_add_u32_e32 v3, s22, v2
	v_add_u32_e32 v4, s22, v3
	v_add_u32_e32 v5, s22, v4
	v_add_u32_e32 v6, s22, v5
	v_add_u32_e32 v7, s22, v6
	v_add_u32_e32 v8, s22, v7
	v_add_u32_e32 v9, s22, v8
	v_and_b32_e32 v24, 15, v0
	v_bfe_u32 v25, v0, 4, 2
	v_lshrrev_b32_e32 v26, 1, v24
	v_xor_b32_e32 v26, v26, v25
	v_lshlrev_b32_e32 v26, 4, v26
	v_bfe_u32 v27, v0, 7, 1
	v_bfe_u32 v28, v0, 6, 1
	v_lshl_add_u32 v29, v27, 6, v24
	v_lshl_add_u32 v10, v29, 7, v26
	v_lshl_add_u32 v30, v28, 7, v24
	v_lshl_add_u32 v11, v30, 7, v26
	v_add_u32_e32 v11, 0x4000, v11
	v_add_u32_e32 v29, s12, v29
	v_lshlrev_b32_e32 v21, 6, v29
	v_mul_u32_u24_e32 v29, 0x1800, v29
	v_lshlrev_b32_e32 v30, 7, v28
	v_lshl_add_u32 v30, v25, 2, v30
	v_add_u32_e32 v30, s13, v30
	v_lshl_add_u32 v16, v30, 1, v29
	s_mov_b32 s22, 0x18000
	v_add_u32_e32 v17, s22, v16
	v_add_u32_e32 v18, s22, v17
	v_add_u32_e32 v19, s22, v18
	s_waitcnt lgkmcnt(0)
	s_mul_i32 s22, s12, 0x600
	s_add_u32 s16, s4, s22
	s_addc_u32 s17, s5, 0
	s_mul_i32 s22, s13, 0x600
	s_add_u32 s18, s6, s22
	s_addc_u32 s19, s7, 0
	s_lshl_b32 s20, s14, 10
	s_mov_b32 s21, 0
	s_add_u32 m0, s20, 0x0
	s_nop 0
	global_load_lds_dwordx4 v2, s[16:17]
	s_add_u32 m0, s20, 0x1000
	s_nop 0
	global_load_lds_dwordx4 v3, s[16:17]
	s_add_u32 m0, s20, 0x2000
	s_nop 0
	global_load_lds_dwordx4 v4, s[16:17]
	s_add_u32 m0, s20, 0x3000
	s_nop 0
	global_load_lds_dwordx4 v5, s[16:17]
	s_add_u32 m0, s20, 0x4000
	s_nop 0
	global_load_lds_dwordx4 v2, s[18:19]
	s_add_u32 m0, s20, 0x5000
	s_nop 0
	global_load_lds_dwordx4 v3, s[18:19]
	s_add_u32 m0, s20, 0x6000
	s_nop 0
	global_load_lds_dwordx4 v4, s[18:19]
	s_add_u32 m0, s20, 0x7000
	s_nop 0
	global_load_lds_dwordx4 v5, s[18:19]
	s_add_u32 m0, s20, 0x8000
	s_nop 0
	global_load_lds_dwordx4 v6, s[18:19]
	s_add_u32 m0, s20, 0x9000
	s_nop 0
	global_load_lds_dwordx4 v7, s[18:19]
	s_add_u32 m0, s20, 0xa000
	s_nop 0
	global_load_lds_dwordx4 v8, s[18:19]
	s_add_u32 m0, s20, 0xb000
	s_nop 0
	global_load_lds_dwordx4 v9, s[18:19]
	s_add_u32 s16, s16, 0x80
	s_addc_u32 s17, s17, 0
	s_add_u32 s18, s18, 0x80
	s_addc_u32 s19, s19, 0
	s_add_u32 s20, s20, 0xc000
	s_sub_u32 s22, s20, 0x24000
	s_cmp_ge_u32 s20, 0x24000
	s_cselect_b32 s20, s22, s20
	s_add_u32 m0, s20, 0x0
	s_nop 0
	global_load_lds_dwordx4 v2, s[16:17]
	s_add_u32 m0, s20, 0x1000
	s_nop 0
	global_load_lds_dwordx4 v3, s[16:17]
	s_add_u32 m0, s20, 0x2000
	s_nop 0
	global_load_lds_dwordx4 v4, s[16:17]
	s_add_u32 m0, s20, 0x3000
	s_nop 0
	global_load_lds_dwordx4 v5, s[16:17]
	s_add_u32 m0, s20, 0x4000
	s_nop 0
	global_load_lds_dwordx4 v2, s[18:19]
	s_add_u32 m0, s20, 0x5000
	s_nop 0
	global_load_lds_dwordx4 v3, s[18:19]
	s_add_u32 m0, s20, 0x6000
	s_nop 0
	global_load_lds_dwordx4 v4, s[18:19]
	s_add_u32 m0, s20, 0x7000
	s_nop 0
	global_load_lds_dwordx4 v5, s[18:19]
	s_add_u32 m0, s20, 0x8000
	s_nop 0
	global_load_lds_dwordx4 v6, s[18:19]
	s_add_u32 m0, s20, 0x9000
	s_nop 0
	global_load_lds_dwordx4 v7, s[18:19]
	s_add_u32 m0, s20, 0xa000
	s_nop 0
	global_load_lds_dwordx4 v8, s[18:19]
	s_add_u32 m0, s20, 0xb000
	s_nop 0
	global_load_lds_dwordx4 v9, s[18:19]
	s_add_u32 s16, s16, 0x80
	s_addc_u32 s17, s17, 0
	s_add_u32 s18, s18, 0x80
	s_addc_u32 s19, s19, 0
	s_add_u32 s20, s20, 0xc000
	s_sub_u32 s22, s20, 0x24000
	s_cmp_ge_u32 s20, 0x24000
	s_cselect_b32 s20, s22, s20
	s_add_u32 m0, s20, 0x0
	s_nop 0
	global_load_lds_dwordx4 v2, s[16:17]
	s_add_u32 m0, s20, 0x1000
	s_nop 0
	global_load_lds_dwordx4 v3, s[16:17]
	s_add_u32 m0, s20, 0x2000
	s_nop 0
	global_load_lds_dwordx4 v4, s[16:17]
	s_add_u32 m0, s20, 0x3000
	s_nop 0
	global_load_lds_dwordx4 v5, s[16:17]
	s_add_u32 m0, s20, 0x4000
	s_nop 0
	global_load_lds_dwordx4 v2, s[18:19]
	s_add_u32 m0, s20, 0x5000
	s_nop 0
	global_load_lds_dwordx4 v3, s[18:19]
	v_mov_b32_e32 v128, 0
	v_mov_b32_e32 v129, 0
	v_mov_b32_e32 v130, 0
	v_mov_b32_e32 v131, 0
	v_mov_b32_e32 v132, 0
	v_mov_b32_e32 v133, 0
	v_mov_b32_e32 v134, 0
	v_mov_b32_e32 v135, 0
	v_mov_b32_e32 v136, 0
	v_mov_b32_e32 v137, 0
	v_mov_b32_e32 v138, 0
	v_mov_b32_e32 v139, 0
	v_mov_b32_e32 v140, 0
	v_mov_b32_e32 v141, 0
	v_mov_b32_e32 v142, 0
	v_mov_b32_e32 v143, 0
	v_mov_b32_e32 v144, 0
	v_mov_b32_e32 v145, 0
	v_mov_b32_e32 v146, 0
	v_mov_b32_e32 v147, 0
	v_mov_b32_e32 v148, 0
	v_mov_b32_e32 v149, 0
	v_mov_b32_e32 v150, 0
	v_mov_b32_e32 v151, 0
	v_mov_b32_e32 v152, 0
	v_mov_b32_e32 v153, 0
	v_mov_b32_e32 v154, 0
	v_mov_b32_e32 v155, 0
	v_mov_b32_e32 v156, 0
	v_mov_b32_e32 v157, 0
	v_mov_b32_e32 v158, 0
	v_mov_b32_e32 v159, 0
	v_mov_b32_e32 v160, 0
	v_mov_b32_e32 v161, 0
	v_mov_b32_e32 v162, 0
	v_mov_b32_e32 v163, 0
	v_mov_b32_e32 v164, 0
	v_mov_b32_e32 v165, 0
	v_mov_b32_e32 v166, 0
	v_mov_b32_e32 v167, 0
	v_mov_b32_e32 v168, 0
	v_mov_b32_e32 v169, 0
	v_mov_b32_e32 v170, 0
	v_mov_b32_e32 v171, 0
	v_mov_b32_e32 v172, 0
	v_mov_b32_e32 v173, 0
	v_mov_b32_e32 v174, 0
	v_mov_b32_e32 v175, 0
	v_mov_b32_e32 v176, 0
	v_mov_b32_e32 v177, 0
	v_mov_b32_e32 v178, 0
	v_mov_b32_e32 v179, 0
	v_mov_b32_e32 v180, 0
	v_mov_b32_e32 v181, 0
	v_mov_b32_e32 v182, 0
	v_mov_b32_e32 v183, 0
	v_mov_b32_e32 v184, 0
	v_mov_b32_e32 v185, 0
	v_mov_b32_e32 v186, 0
	v_mov_b32_e32 v187, 0
	v_mov_b32_e32 v188, 0
	v_mov_b32_e32 v189, 0
	v_mov_b32_e32 v190, 0
	v_mov_b32_e32 v191, 0
	v_mov_b32_e32 v192, 0
	v_mov_b32_e32 v193, 0
	v_mov_b32_e32 v194, 0
	v_mov_b32_e32 v195, 0
	v_mov_b32_e32 v196, 0
	v_mov_b32_e32 v197, 0
	v_mov_b32_e32 v198, 0
	v_mov_b32_e32 v199, 0
	v_mov_b32_e32 v200, 0
	v_mov_b32_e32 v201, 0
	v_mov_b32_e32 v202, 0
	v_mov_b32_e32 v203, 0
	v_mov_b32_e32 v204, 0
	v_mov_b32_e32 v205, 0
	v_mov_b32_e32 v206, 0
	v_mov_b32_e32 v207, 0
	v_mov_b32_e32 v208, 0
	v_mov_b32_e32 v209, 0
	v_mov_b32_e32 v210, 0
	v_mov_b32_e32 v211, 0
	v_mov_b32_e32 v212, 0
	v_mov_b32_e32 v213, 0
	v_mov_b32_e32 v214, 0
	v_mov_b32_e32 v215, 0
	v_mov_b32_e32 v216, 0
	v_mov_b32_e32 v217, 0
	v_mov_b32_e32 v218, 0
	v_mov_b32_e32 v219, 0
	v_mov_b32_e32 v220, 0
	v_mov_b32_e32 v221, 0
	v_mov_b32_e32 v222, 0
	v_mov_b32_e32 v223, 0
	v_mov_b32_e32 v224, 0
	v_mov_b32_e32 v225, 0
	v_mov_b32_e32 v226, 0
	v_mov_b32_e32 v227, 0
	v_mov_b32_e32 v228, 0
	v_mov_b32_e32 v229, 0
	v_mov_b32_e32 v230, 0
	v_mov_b32_e32 v231, 0
	v_mov_b32_e32 v232, 0
	v_mov_b32_e32 v233, 0
	v_mov_b32_e32 v234, 0
	v_mov_b32_e32 v235, 0
	v_mov_b32_e32 v236, 0
	v_mov_b32_e32 v237, 0
	v_mov_b32_e32 v238, 0
	v_mov_b32_e32 v239, 0
	v_mov_b32_e32 v240, 0
	v_mov_b32_e32 v241, 0
	v_mov_b32_e32 v242, 0
	v_mov_b32_e32 v243, 0
	v_mov_b32_e32 v244, 0
	v_mov_b32_e32 v245, 0
	v_mov_b32_e32 v246, 0
	v_mov_b32_e32 v247, 0
	v_mov_b32_e32 v248, 0
	v_mov_b32_e32 v249, 0
	v_mov_b32_e32 v250, 0
	v_mov_b32_e32 v251, 0
	v_mov_b32_e32 v252, 0
	v_mov_b32_e32 v253, 0
	v_mov_b32_e32 v254, 0
	v_mov_b32_e32 v255, 0
	s_waitcnt vmcnt(18)
	s_barrier
	v_add_u32_e32 v12, s21, v10
	v_add_u32_e32 v14, s21, v11
	v_xor_b32_e32 v13, 64, v12
	v_xor_b32_e32 v15, 64, v14
	s_add_u32 s21, s21, 0xc000
	s_sub_u32 s23, s21, 0x24000
	s_cmp_ge_u32 s21, 0x24000
	s_cselect_b32 s21, s23, s21
	ds_read_b128 v[32:35], v12 offset:0
	ds_read_b128 v[36:39], v12 offset:2048
	ds_read_b128 v[40:43], v12 offset:4096
	ds_read_b128 v[44:47], v12 offset:6144
	ds_read_b128 v[48:51], v14 offset:0
	ds_read_b128 v[52:55], v14 offset:2048
	ds_read_b128 v[56:59], v14 offset:4096
	ds_read_b128 v[60:63], v14 offset:6144
	ds_read_b128 v[64:67], v14 offset:8192
	ds_read_b128 v[68:71], v14 offset:10240
	ds_read_b128 v[72:75], v14 offset:12288
	ds_read_b128 v[76:79], v14 offset:14336
	s_mov_b32 s15, 0
.Lup_loop:
	s_waitcnt lgkmcnt(0)
	v_mfma_f32_16x16x32_bf16 v[128:131], v[48:51], v[32:35], v[128:131]
	ds_read_b128 v[80:83], v13 offset:0
	v_mfma_f32_16x16x32_bf16 v[132:135], v[48:51], v[36:39], v[132:135]
	s_add_u32 m0, s20, 0x6000
	v_mfma_f32_16x16x32_bf16 v[136:139], v[48:51], v[40:43], v[136:139]
	ds_read_b128 v[84:87], v13 offset:2048
	v_mfma_f32_16x16x32_bf16 v[140:143], v[48:51], v[44:47], v[140:143]
	global_load_lds_dwordx4 v4, s[18:19]
	v_mfma_f32_16x16x32_bf16 v[144:147], v[52:55], v[32:35], v[144:147]
	ds_read_b128 v[88:91], v13 offset:4096
	v_mfma_f32_16x16x32_bf16 v[148:151], v[52:55], v[36:39], v[148:151]
	s_add_u32 m0, s20, 0x7000
	v_mfma_f32_16x16x32_bf16 v[152:155], v[52:55], v[40:43], v[152:155]
	ds_read_b128 v[92:95], v13 offset:6144
	v_mfma_f32_16x16x32_bf16 v[156:159], v[52:55], v[44:47], v[156:159]
	global_load_lds_dwordx4 v5, s[18:19]
	v_mfma_f32_16x16x32_bf16 v[160:163], v[56:59], v[32:35], v[160:163]
	ds_read_b128 v[96:99], v15 offset:0
	v_mfma_f32_16x16x32_bf16 v[164:167], v[56:59], v[36:39], v[164:167]
	s_add_u32 m0, s20, 0x8000
	v_mfma_f32_16x16x32_bf16 v[168:171], v[56:59], v[40:43], v[168:171]
	ds_read_b128 v[100:103], v15 offset:2048
	v_mfma_f32_16x16x32_bf16 v[172:175], v[56:59], v[44:47], v[172:175]
	global_load_lds_dwordx4 v6, s[18:19]
	v_mfma_f32_16x16x32_bf16 v[176:179], v[60:63], v[32:35], v[176:179]
	ds_read_b128 v[104:107], v15 offset:4096
	v_mfma_f32_16x16x32_bf16 v[180:183], v[60:63], v[36:39], v[180:183]
	s_add_u32 m0, s20, 0x9000
	v_mfma_f32_16x16x32_bf16 v[184:187], v[60:63], v[40:43], v[184:187]
	ds_read_b128 v[108:111], v15 offset:6144
	v_mfma_f32_16x16x32_bf16 v[188:191], v[60:63], v[44:47], v[188:191]
	global_load_lds_dwordx4 v7, s[18:19]
	v_mfma_f32_16x16x32_bf16 v[192:195], v[64:67], v[32:35], v[192:195]
	ds_read_b128 v[112:115], v15 offset:8192
	v_mfma_f32_16x16x32_bf16 v[196:199], v[64:67], v[36:39], v[196:199]
	s_add_u32 m0, s20, 0xa000
	v_mfma_f32_16x16x32_bf16 v[200:203], v[64:67], v[40:43], v[200:203]
	ds_read_b128 v[116:119], v15 offset:10240
	v_mfma_f32_16x16x32_bf16 v[204:207], v[64:67], v[44:47], v[204:207]
	global_load_lds_dwordx4 v8, s[18:19]
	v_mfma_f32_16x16x32_bf16 v[208:211], v[68:71], v[32:35], v[208:211]
	ds_read_b128 v[120:123], v15 offset:12288
	v_mfma_f32_16x16x32_bf16 v[212:215], v[68:71], v[36:39], v[212:215]
	s_add_u32 m0, s20, 0xb000
	v_mfma_f32_16x16x32_bf16 v[216:219], v[68:71], v[40:43], v[216:219]
	ds_read_b128 v[124:127], v15 offset:14336
	v_mfma_f32_16x16x32_bf16 v[220:223], v[68:71], v[44:47], v[220:223]
	global_load_lds_dwordx4 v9, s[18:19]
	v_mfma_f32_16x16x32_bf16 v[224:227], v[72:75], v[32:35], v[224:227]
	v_mfma_f32_16x16x32_bf16 v[228:231], v[72:75], v[36:39], v[228:231]
	v_mfma_f32_16x16x32_bf16 v[232:235], v[72:75], v[40:43], v[232:235]
	v_mfma_f32_16x16x32_bf16 v[236:239], v[72:75], v[44:47], v[236:239]
	v_mfma_f32_16x16x32_bf16 v[240:243], v[76:79], v[32:35], v[240:243]
	s_add_u32 s16, s16, 0x80
	s_addc_u32 s17, s17, 0
	s_add_u32 s18, s18, 0x80
	s_addc_u32 s19, s19, 0
	v_mfma_f32_16x16x32_bf16 v[244:247], v[76:79], v[36:39], v[244:247]
	s_add_u32 s20, s20, 0xc000
	s_sub_u32 s22, s20, 0x24000
	s_cmp_ge_u32 s20, 0x24000
	s_cselect_b32 s20, s22, s20
	v_mfma_f32_16x16x32_bf16 v[248:251], v[76:79], v[40:43], v[248:251]
	v_add_u32_e32 v12, s21, v10
	v_add_u32_e32 v14, s21, v11
	v_xor_b32_e32 v13, 64, v12
	v_xor_b32_e32 v15, 64, v14
	v_mfma_f32_16x16x32_bf16 v[252:255], v[76:79], v[44:47], v[252:255]
	s_add_u32 s21, s21, 0xc000
	s_sub_u32 s23, s21, 0x24000
	s_cmp_ge_u32 s21, 0x24000
	s_cselect_b32 s21, s23, s21
	s_waitcnt vmcnt(12) lgkmcnt(0)
	s_barrier
	v_mfma_f32_16x16x32_bf16 v[128:131], v[96:99], v[80:83], v[128:131]
	ds_read_b128 v[32:35], v12 offset:0
	v_mfma_f32_16x16x32_bf16 v[132:135], v[96:99], v[84:87], v[132:135]
	s_add_u32 m0, s20, 0x0
	v_mfma_f32_16x16x32_bf16 v[136:139], v[96:99], v[88:91], v[136:139]
	ds_read_b128 v[36:39], v12 offset:2048
	v_mfma_f32_16x16x32_bf16 v[140:143], v[96:99], v[92:95], v[140:143]
	global_load_lds_dwordx4 v2, s[16:17]
	v_mfma_f32_16x16x32_bf16 v[144:147], v[100:103], v[80:83], v[144:147]
	ds_read_b128 v[40:43], v12 offset:4096
	v_mfma_f32_16x16x32_bf16 v[148:151], v[100:103], v[84:87], v[148:151]
	s_add_u32 m0, s20, 0x1000
	v_mfma_f32_16x16x32_bf16 v[152:155], v[100:103], v[88:91], v[152:155]
	ds_read_b128 v[44:47], v12 offset:6144
	v_mfma_f32_16x16x32_bf16 v[156:159], v[100:103], v[92:95], v[156:159]
	global_load_lds_dwordx4 v3, s[16:17]
	v_mfma_f32_16x16x32_bf16 v[160:163], v[104:107], v[80:83], v[160:163]
	ds_read_b128 v[48:51], v14 offset:0
	v_mfma_f32_16x16x32_bf16 v[164:167], v[104:107], v[84:87], v[164:167]
	s_add_u32 m0, s20, 0x2000
	v_mfma_f32_16x16x32_bf16 v[168:171], v[104:107], v[88:91], v[168:171]
	ds_read_b128 v[52:55], v14 offset:2048
	v_mfma_f32_16x16x32_bf16 v[172:175], v[104:107], v[92:95], v[172:175]
	global_load_lds_dwordx4 v4, s[16:17]
	v_mfma_f32_16x16x32_bf16 v[176:179], v[108:111], v[80:83], v[176:179]
	ds_read_b128 v[56:59], v14 offset:4096
	v_mfma_f32_16x16x32_bf16 v[180:183], v[108:111], v[84:87], v[180:183]
	s_add_u32 m0, s20, 0x3000
	v_mfma_f32_16x16x32_bf16 v[184:187], v[108:111], v[88:91], v[184:187]
	ds_read_b128 v[60:63], v14 offset:6144
	v_mfma_f32_16x16x32_bf16 v[188:191], v[108:111], v[92:95], v[188:191]
	global_load_lds_dwordx4 v5, s[16:17]
	v_mfma_f32_16x16x32_bf16 v[192:195], v[112:115], v[80:83], v[192:195]
	ds_read_b128 v[64:67], v14 offset:8192
	v_mfma_f32_16x16x32_bf16 v[196:199], v[112:115], v[84:87], v[196:199]
	s_add_u32 m0, s20, 0x4000
	v_mfma_f32_16x16x32_bf16 v[200:203], v[112:115], v[88:91], v[200:203]
	ds_read_b128 v[68:71], v14 offset:10240
	v_mfma_f32_16x16x32_bf16 v[204:207], v[112:115], v[92:95], v[204:207]
	global_load_lds_dwordx4 v2, s[18:19]
	v_mfma_f32_16x16x32_bf16 v[208:211], v[116:119], v[80:83], v[208:211]
	ds_read_b128 v[72:75], v14 offset:12288
	v_mfma_f32_16x16x32_bf16 v[212:215], v[116:119], v[84:87], v[212:215]
	s_add_u32 m0, s20, 0x5000
	v_mfma_f32_16x16x32_bf16 v[216:219], v[116:119], v[88:91], v[216:219]
	ds_read_b128 v[76:79], v14 offset:14336
	v_mfma_f32_16x16x32_bf16 v[220:223], v[116:119], v[92:95], v[220:223]
	global_load_lds_dwordx4 v3, s[18:19]
	v_mfma_f32_16x16x32_bf16 v[224:227], v[120:123], v[80:83], v[224:227]
	v_mfma_f32_16x16x32_bf16 v[228:231], v[120:123], v[84:87], v[228:231]
	v_mfma_f32_16x16x32_bf16 v[232:235], v[120:123], v[88:91], v[232:235]
	v_mfma_f32_16x16x32_bf16 v[236:239], v[120:123], v[92:95], v[236:239]
	v_mfma_f32_16x16x32_bf16 v[240:243], v[124:127], v[80:83], v[240:243]
	v_mfma_f32_16x16x32_bf16 v[244:247], v[124:127], v[84:87], v[244:247]
	v_mfma_f32_16x16x32_bf16 v[248:251], v[124:127], v[88:91], v[248:251]
	v_mfma_f32_16x16x32_bf16 v[252:255], v[124:127], v[92:95], v[252:255]
	s_add_u32 s15, s15, 1
	s_cmp_lt_u32 s15, 9
	s_cbranch_scc1 .Lup_loop
	s_waitcnt lgkmcnt(0)
	v_mfma_f32_16x16x32_bf16 v[128:131], v[48:51], v[32:35], v[128:131]
	ds_read_b128 v[80:83], v13 offset:0
	v_mfma_f32_16x16x32_bf16 v[132:135], v[48:51], v[36:39], v[132:135]
	s_add_u32 m0, s20, 0x6000
	v_mfma_f32_16x16x32_bf16 v[136:139], v[48:51], v[40:43], v[136:139]
	ds_read_b128 v[84:87], v13 offset:2048
	v_mfma_f32_16x16x32_bf16 v[140:143], v[48:51], v[44:47], v[140:143]
	global_load_lds_dwordx4 v4, s[18:19]
	v_mfma_f32_16x16x32_bf16 v[144:147], v[52:55], v[32:35], v[144:147]
	ds_read_b128 v[88:91], v13 offset:4096
	v_mfma_f32_16x16x32_bf16 v[148:151], v[52:55], v[36:39], v[148:151]
	s_add_u32 m0, s20, 0x7000
	v_mfma_f32_16x16x32_bf16 v[152:155], v[52:55], v[40:43], v[152:155]
	ds_read_b128 v[92:95], v13 offset:6144
	v_mfma_f32_16x16x32_bf16 v[156:159], v[52:55], v[44:47], v[156:159]
	global_load_lds_dwordx4 v5, s[18:19]
	v_mfma_f32_16x16x32_bf16 v[160:163], v[56:59], v[32:35], v[160:163]
	ds_read_b128 v[96:99], v15 offset:0
	v_mfma_f32_16x16x32_bf16 v[164:167], v[56:59], v[36:39], v[164:167]
	s_add_u32 m0, s20, 0x8000
	v_mfma_f32_16x16x32_bf16 v[168:171], v[56:59], v[40:43], v[168:171]
	ds_read_b128 v[100:103], v15 offset:2048
	v_mfma_f32_16x16x32_bf16 v[172:175], v[56:59], v[44:47], v[172:175]
	global_load_lds_dwordx4 v6, s[18:19]
	v_mfma_f32_16x16x32_bf16 v[176:179], v[60:63], v[32:35], v[176:179]
	ds_read_b128 v[104:107], v15 offset:4096
	v_mfma_f32_16x16x32_bf16 v[180:183], v[60:63], v[36:39], v[180:183]
	s_add_u32 m0, s20, 0x9000
	v_mfma_f32_16x16x32_bf16 v[184:187], v[60:63], v[40:43], v[184:187]
	ds_read_b128 v[108:111], v15 offset:6144
	v_mfma_f32_16x16x32_bf16 v[188:191], v[60:63], v[44:47], v[188:191]
	global_load_lds_dwordx4 v7, s[18:19]
	v_mfma_f32_16x16x32_bf16 v[192:195], v[64:67], v[32:35], v[192:195]
	ds_read_b128 v[112:115], v15 offset:8192
	v_mfma_f32_16x16x32_bf16 v[196:199], v[64:67], v[36:39], v[196:199]
	s_add_u32 m0, s20, 0xa000
	v_mfma_f32_16x16x32_bf16 v[200:203], v[64:67], v[40:43], v[200:203]
	ds_read_b128 v[116:119], v15 offset:10240
	v_mfma_f32_16x16x32_bf16 v[204:207], v[64:67], v[44:47], v[204:207]
	global_load_lds_dwordx4 v8, s[18:19]
	v_mfma_f32_16x16x32_bf16 v[208:211], v[68:71], v[32:35], v[208:211]
	ds_read_b128 v[120:123], v15 offset:12288
	v_mfma_f32_16x16x32_bf16 v[212:215], v[68:71], v[36:39], v[212:215]
	s_add_u32 m0, s20, 0xb000
	v_mfma_f32_16x16x32_bf16 v[216:219], v[68:71], v[40:43], v[216:219]
	ds_read_b128 v[124:127], v15 offset:14336
	v_mfma_f32_16x16x32_bf16 v[220:223], v[68:71], v[44:47], v[220:223]
	global_load_lds_dwordx4 v9, s[18:19]
	v_mfma_f32_16x16x32_bf16 v[224:227], v[72:75], v[32:35], v[224:227]
	v_mfma_f32_16x16x32_bf16 v[228:231], v[72:75], v[36:39], v[228:231]
	v_mfma_f32_16x16x32_bf16 v[232:235], v[72:75], v[40:43], v[232:235]
	v_mfma_f32_16x16x32_bf16 v[236:239], v[72:75], v[44:47], v[236:239]
	v_mfma_f32_16x16x32_bf16 v[240:243], v[76:79], v[32:35], v[240:243]
	s_add_u32 s16, s16, 0x80
	s_addc_u32 s17, s17, 0
	s_add_u32 s18, s18, 0x80
	s_addc_u32 s19, s19, 0
	v_mfma_f32_16x16x32_bf16 v[244:247], v[76:79], v[36:39], v[244:247]
	s_add_u32 s20, s20, 0xc000
	s_sub_u32 s22, s20, 0x24000
	s_cmp_ge_u32 s20, 0x24000
	s_cselect_b32 s20, s22, s20
	v_mfma_f32_16x16x32_bf16 v[248:251], v[76:79], v[40:43], v[248:251]
	v_add_u32_e32 v12, s21, v10
	v_add_u32_e32 v14, s21, v11
	v_xor_b32_e32 v13, 64, v12
	v_xor_b32_e32 v15, 64, v14
	v_mfma_f32_16x16x32_bf16 v[252:255], v[76:79], v[44:47], v[252:255]
	s_add_u32 s21, s21, 0xc000
	s_sub_u32 s23, s21, 0x24000
	s_cmp_ge_u32 s21, 0x24000
	s_cselect_b32 s21, s23, s21
	s_waitcnt vmcnt(12) lgkmcnt(0)
	s_barrier
	v_mfma_f32_16x16x32_bf16 v[128:131], v[96:99], v[80:83], v[128:131]
	ds_read_b128 v[32:35], v12 offset:0
	v_mfma_f32_16x16x32_bf16 v[132:135], v[96:99], v[84:87], v[132:135]
	ds_read_b128 v[36:39], v12 offset:2048
	v_mfma_f32_16x16x32_bf16 v[136:139], v[96:99], v[88:91], v[136:139]
	ds_read_b128 v[40:43], v12 offset:4096
	v_mfma_f32_16x16x32_bf16 v[140:143], v[96:99], v[92:95], v[140:143]
	ds_read_b128 v[44:47], v12 offset:6144
	v_mfma_f32_16x16x32_bf16 v[144:147], v[100:103], v[80:83], v[144:147]
	ds_read_b128 v[48:51], v14 offset:0
	v_mfma_f32_16x16x32_bf16 v[148:151], v[100:103], v[84:87], v[148:151]
	ds_read_b128 v[52:55], v14 offset:2048
	v_mfma_f32_16x16x32_bf16 v[152:155], v[100:103], v[88:91], v[152:155]
	ds_read_b128 v[56:59], v14 offset:4096
	v_mfma_f32_16x16x32_bf16 v[156:159], v[100:103], v[92:95], v[156:159]
	ds_read_b128 v[60:63], v14 offset:6144
	v_mfma_f32_16x16x32_bf16 v[160:163], v[104:107], v[80:83], v[160:163]
	ds_read_b128 v[64:67], v14 offset:8192
	v_mfma_f32_16x16x32_bf16 v[164:167], v[104:107], v[84:87], v[164:167]
	ds_read_b128 v[68:71], v14 offset:10240
	v_mfma_f32_16x16x32_bf16 v[168:171], v[104:107], v[88:91], v[168:171]
	ds_read_b128 v[72:75], v14 offset:12288
	v_mfma_f32_16x16x32_bf16 v[172:175], v[104:107], v[92:95], v[172:175]
	ds_read_b128 v[76:79], v14 offset:14336
	v_mfma_f32_16x16x32_bf16 v[176:179], v[108:111], v[80:83], v[176:179]
	v_mfma_f32_16x16x32_bf16 v[180:183], v[108:111], v[84:87], v[180:183]
	v_mfma_f32_16x16x32_bf16 v[184:187], v[108:111], v[88:91], v[184:187]
	v_mfma_f32_16x16x32_bf16 v[188:191], v[108:111], v[92:95], v[188:191]
	v_mfma_f32_16x16x32_bf16 v[192:195], v[112:115], v[80:83], v[192:195]
	v_mfma_f32_16x16x32_bf16 v[196:199], v[112:115], v[84:87], v[196:199]
	v_mfma_f32_16x16x32_bf16 v[200:203], v[112:115], v[88:91], v[200:203]
	v_mfma_f32_16x16x32_bf16 v[204:207], v[112:115], v[92:95], v[204:207]
	v_mfma_f32_16x16x32_bf16 v[208:211], v[116:119], v[80:83], v[208:211]
	v_mfma_f32_16x16x32_bf16 v[212:215], v[116:119], v[84:87], v[212:215]
	v_mfma_f32_16x16x32_bf16 v[216:219], v[116:119], v[88:91], v[216:219]
	v_mfma_f32_16x16x32_bf16 v[220:223], v[116:119], v[92:95], v[220:223]
	v_mfma_f32_16x16x32_bf16 v[224:227], v[120:123], v[80:83], v[224:227]
	v_mfma_f32_16x16x32_bf16 v[228:231], v[120:123], v[84:87], v[228:231]
	v_mfma_f32_16x16x32_bf16 v[232:235], v[120:123], v[88:91], v[232:235]
	v_mfma_f32_16x16x32_bf16 v[236:239], v[120:123], v[92:95], v[236:239]
	v_mfma_f32_16x16x32_bf16 v[240:243], v[124:127], v[80:83], v[240:243]
	v_mfma_f32_16x16x32_bf16 v[244:247], v[124:127], v[84:87], v[244:247]
	v_mfma_f32_16x16x32_bf16 v[248:251], v[124:127], v[88:91], v[248:251]
	v_mfma_f32_16x16x32_bf16 v[252:255], v[124:127], v[92:95], v[252:255]
	s_waitcnt lgkmcnt(0)
	v_mfma_f32_16x16x32_bf16 v[128:131], v[48:51], v[32:35], v[128:131]
	ds_read_b128 v[80:83], v13 offset:0
	v_mfma_f32_16x16x32_bf16 v[132:135], v[48:51], v[36:39], v[132:135]
	ds_read_b128 v[84:87], v13 offset:2048
	v_mfma_f32_16x16x32_bf16 v[136:139], v[48:51], v[40:43], v[136:139]
	ds_read_b128 v[88:91], v13 offset:4096
	v_mfma_f32_16x16x32_bf16 v[140:143], v[48:51], v[44:47], v[140:143]
	ds_read_b128 v[92:95], v13 offset:6144
	v_mfma_f32_16x16x32_bf16 v[144:147], v[52:55], v[32:35], v[144:147]
	ds_read_b128 v[96:99], v15 offset:0
	v_mfma_f32_16x16x32_bf16 v[148:151], v[52:55], v[36:39], v[148:151]
	ds_read_b128 v[100:103], v15 offset:2048
	v_mfma_f32_16x16x32_bf16 v[152:155], v[52:55], v[40:43], v[152:155]
	ds_read_b128 v[104:107], v15 offset:4096
	v_mfma_f32_16x16x32_bf16 v[156:159], v[52:55], v[44:47], v[156:159]
	ds_read_b128 v[108:111], v15 offset:6144
	v_mfma_f32_16x16x32_bf16 v[160:163], v[56:59], v[32:35], v[160:163]
	ds_read_b128 v[112:115], v15 offset:8192
	v_mfma_f32_16x16x32_bf16 v[164:167], v[56:59], v[36:39], v[164:167]
	ds_read_b128 v[116:119], v15 offset:10240
	v_mfma_f32_16x16x32_bf16 v[168:171], v[56:59], v[40:43], v[168:171]
	ds_read_b128 v[120:123], v15 offset:12288
	v_mfma_f32_16x16x32_bf16 v[172:175], v[56:59], v[44:47], v[172:175]
	ds_read_b128 v[124:127], v15 offset:14336
	v_mfma_f32_16x16x32_bf16 v[176:179], v[60:63], v[32:35], v[176:179]
	v_mfma_f32_16x16x32_bf16 v[180:183], v[60:63], v[36:39], v[180:183]
	v_mfma_f32_16x16x32_bf16 v[184:187], v[60:63], v[40:43], v[184:187]
	v_mfma_f32_16x16x32_bf16 v[188:191], v[60:63], v[44:47], v[188:191]
	v_mfma_f32_16x16x32_bf16 v[192:195], v[64:67], v[32:35], v[192:195]
	v_mfma_f32_16x16x32_bf16 v[196:199], v[64:67], v[36:39], v[196:199]
	v_mfma_f32_16x16x32_bf16 v[200:203], v[64:67], v[40:43], v[200:203]
	v_mfma_f32_16x16x32_bf16 v[204:207], v[64:67], v[44:47], v[204:207]
	v_mfma_f32_16x16x32_bf16 v[208:211], v[68:71], v[32:35], v[208:211]
	v_mfma_f32_16x16x32_bf16 v[212:215], v[68:71], v[36:39], v[212:215]
	v_mfma_f32_16x16x32_bf16 v[216:219], v[68:71], v[40:43], v[216:219]
	v_mfma_f32_16x16x32_bf16 v[220:223], v[68:71], v[44:47], v[220:223]
	v_mfma_f32_16x16x32_bf16 v[224:227], v[72:75], v[32:35], v[224:227]
	v_mfma_f32_16x16x32_bf16 v[228:231], v[72:75], v[36:39], v[228:231]
	v_mfma_f32_16x16x32_bf16 v[232:235], v[72:75], v[40:43], v[232:235]
	v_mfma_f32_16x16x32_bf16 v[236:239], v[72:75], v[44:47], v[236:239]
	v_mfma_f32_16x16x32_bf16 v[240:243], v[76:79], v[32:35], v[240:243]
	v_add_u32_e32 v12, s21, v10
	v_add_u32_e32 v14, s21, v11
	v_xor_b32_e32 v13, 64, v12
	v_xor_b32_e32 v15, 64, v14
	v_mfma_f32_16x16x32_bf16 v[244:247], v[76:79], v[36:39], v[244:247]
	s_add_u32 s21, s21, 0xc000
	s_sub_u32 s23, s21, 0x24000
	s_cmp_ge_u32 s21, 0x24000
	s_cselect_b32 s21, s23, s21
	v_mfma_f32_16x16x32_bf16 v[248:251], v[76:79], v[40:43], v[248:251]
	v_mfma_f32_16x16x32_bf16 v[252:255], v[76:79], v[44:47], v[252:255]
	s_waitcnt vmcnt(0) lgkmcnt(0)
	s_barrier
	v_mfma_f32_16x16x32_bf16 v[128:131], v[96:99], v[80:83], v[128:131]
	ds_read_b128 v[32:35], v12 offset:0
	v_mfma_f32_16x16x32_bf16 v[132:135], v[96:99], v[84:87], v[132:135]
	ds_read_b128 v[36:39], v12 offset:2048
	v_mfma_f32_16x16x32_bf16 v[136:139], v[96:99], v[88:91], v[136:139]
	ds_read_b128 v[40:43], v12 offset:4096
	v_mfma_f32_16x16x32_bf16 v[140:143], v[96:99], v[92:95], v[140:143]
	ds_read_b128 v[44:47], v12 offset:6144
	v_mfma_f32_16x16x32_bf16 v[144:147], v[100:103], v[80:83], v[144:147]
	ds_read_b128 v[48:51], v14 offset:0
	v_mfma_f32_16x16x32_bf16 v[148:151], v[100:103], v[84:87], v[148:151]
	ds_read_b128 v[52:55], v14 offset:2048
	v_mfma_f32_16x16x32_bf16 v[152:155], v[100:103], v[88:91], v[152:155]
	ds_read_b128 v[56:59], v14 offset:4096
	v_mfma_f32_16x16x32_bf16 v[156:159], v[100:103], v[92:95], v[156:159]
	ds_read_b128 v[60:63], v14 offset:6144
	v_mfma_f32_16x16x32_bf16 v[160:163], v[104:107], v[80:83], v[160:163]
	ds_read_b128 v[64:67], v14 offset:8192
	v_mfma_f32_16x16x32_bf16 v[164:167], v[104:107], v[84:87], v[164:167]
	ds_read_b128 v[68:71], v14 offset:10240
	v_mfma_f32_16x16x32_bf16 v[168:171], v[104:107], v[88:91], v[168:171]
	ds_read_b128 v[72:75], v14 offset:12288
	v_mfma_f32_16x16x32_bf16 v[172:175], v[104:107], v[92:95], v[172:175]
	ds_read_b128 v[76:79], v14 offset:14336
	v_mfma_f32_16x16x32_bf16 v[176:179], v[108:111], v[80:83], v[176:179]
	v_mfma_f32_16x16x32_bf16 v[180:183], v[108:111], v[84:87], v[180:183]
	v_mfma_f32_16x16x32_bf16 v[184:187], v[108:111], v[88:91], v[184:187]
	v_mfma_f32_16x16x32_bf16 v[188:191], v[108:111], v[92:95], v[188:191]
	v_mfma_f32_16x16x32_bf16 v[192:195], v[112:115], v[80:83], v[192:195]
	v_mfma_f32_16x16x32_bf16 v[196:199], v[112:115], v[84:87], v[196:199]
	v_mfma_f32_16x16x32_bf16 v[200:203], v[112:115], v[88:91], v[200:203]
	v_mfma_f32_16x16x32_bf16 v[204:207], v[112:115], v[92:95], v[204:207]
	v_mfma_f32_16x16x32_bf16 v[208:211], v[116:119], v[80:83], v[208:211]
	v_mfma_f32_16x16x32_bf16 v[212:215], v[116:119], v[84:87], v[212:215]
	v_mfma_f32_16x16x32_bf16 v[216:219], v[116:119], v[88:91], v[216:219]
	v_mfma_f32_16x16x32_bf16 v[220:223], v[116:119], v[92:95], v[220:223]
	v_mfma_f32_16x16x32_bf16 v[224:227], v[120:123], v[80:83], v[224:227]
	v_mfma_f32_16x16x32_bf16 v[228:231], v[120:123], v[84:87], v[228:231]
	v_mfma_f32_16x16x32_bf16 v[232:235], v[120:123], v[88:91], v[232:235]
	v_mfma_f32_16x16x32_bf16 v[236:239], v[120:123], v[92:95], v[236:239]
	v_mfma_f32_16x16x32_bf16 v[240:243], v[124:127], v[80:83], v[240:243]
	v_mfma_f32_16x16x32_bf16 v[244:247], v[124:127], v[84:87], v[244:247]
	v_mfma_f32_16x16x32_bf16 v[248:251], v[124:127], v[88:91], v[248:251]
	v_mfma_f32_16x16x32_bf16 v[252:255], v[124:127], v[92:95], v[252:255]
	s_waitcnt lgkmcnt(0)
	v_mfma_f32_16x16x32_bf16 v[128:131], v[48:51], v[32:35], v[128:131]
	ds_read_b128 v[80:83], v13 offset:0
	v_mfma_f32_16x16x32_bf16 v[132:135], v[48:51], v[36:39], v[132:135]
	ds_read_b128 v[84:87], v13 offset:2048
	v_mfma_f32_16x16x32_bf16 v[136:139], v[48:51], v[40:43], v[136:139]
	ds_read_b128 v[88:91], v13 offset:4096
	v_mfma_f32_16x16x32_bf16 v[140:143], v[48:51], v[44:47], v[140:143]
	ds_read_b128 v[92:95], v13 offset:6144
	v_mfma_f32_16x16x32_bf16 v[144:147], v[52:55], v[32:35], v[144:147]
	ds_read_b128 v[96:99], v15 offset:0
	v_mfma_f32_16x16x32_bf16 v[148:151], v[52:55], v[36:39], v[148:151]
	ds_read_b128 v[100:103], v15 offset:2048
	v_mfma_f32_16x16x32_bf16 v[152:155], v[52:55], v[40:43], v[152:155]
	ds_read_b128 v[104:107], v15 offset:4096
	v_mfma_f32_16x16x32_bf16 v[156:159], v[52:55], v[44:47], v[156:159]
	ds_read_b128 v[108:111], v15 offset:6144
	v_mfma_f32_16x16x32_bf16 v[160:163], v[56:59], v[32:35], v[160:163]
	ds_read_b128 v[112:115], v15 offset:8192
	v_mfma_f32_16x16x32_bf16 v[164:167], v[56:59], v[36:39], v[164:167]
	ds_read_b128 v[116:119], v15 offset:10240
	v_mfma_f32_16x16x32_bf16 v[168:171], v[56:59], v[40:43], v[168:171]
	ds_read_b128 v[120:123], v15 offset:12288
	v_mfma_f32_16x16x32_bf16 v[172:175], v[56:59], v[44:47], v[172:175]
	ds_read_b128 v[124:127], v15 offset:14336
	v_mfma_f32_16x16x32_bf16 v[176:179], v[60:63], v[32:35], v[176:179]
	v_mfma_f32_16x16x32_bf16 v[180:183], v[60:63], v[36:39], v[180:183]
	v_mfma_f32_16x16x32_bf16 v[184:187], v[60:63], v[40:43], v[184:187]
	v_mfma_f32_16x16x32_bf16 v[188:191], v[60:63], v[44:47], v[188:191]
	v_mfma_f32_16x16x32_bf16 v[192:195], v[64:67], v[32:35], v[192:195]
	v_mfma_f32_16x16x32_bf16 v[196:199], v[64:67], v[36:39], v[196:199]
	v_mfma_f32_16x16x32_bf16 v[200:203], v[64:67], v[40:43], v[200:203]
	v_mfma_f32_16x16x32_bf16 v[204:207], v[64:67], v[44:47], v[204:207]
	v_mfma_f32_16x16x32_bf16 v[208:211], v[68:71], v[32:35], v[208:211]
	v_mfma_f32_16x16x32_bf16 v[212:215], v[68:71], v[36:39], v[212:215]
	v_mfma_f32_16x16x32_bf16 v[216:219], v[68:71], v[40:43], v[216:219]
	v_mfma_f32_16x16x32_bf16 v[220:223], v[68:71], v[44:47], v[220:223]
	v_mfma_f32_16x16x32_bf16 v[224:227], v[72:75], v[32:35], v[224:227]
	v_mfma_f32_16x16x32_bf16 v[228:231], v[72:75], v[36:39], v[228:231]
	v_mfma_f32_16x16x32_bf16 v[232:235], v[72:75], v[40:43], v[232:235]
	v_mfma_f32_16x16x32_bf16 v[236:239], v[72:75], v[44:47], v[236:239]
	v_mfma_f32_16x16x32_bf16 v[240:243], v[76:79], v[32:35], v[240:243]
	v_mfma_f32_16x16x32_bf16 v[244:247], v[76:79], v[36:39], v[244:247]
	v_mfma_f32_16x16x32_bf16 v[248:251], v[76:79], v[40:43], v[248:251]
	v_mfma_f32_16x16x32_bf16 v[252:255], v[76:79], v[44:47], v[252:255]
	s_waitcnt lgkmcnt(0)
	v_mfma_f32_16x16x32_bf16 v[128:131], v[96:99], v[80:83], v[128:131]
	v_mfma_f32_16x16x32_bf16 v[132:135], v[96:99], v[84:87], v[132:135]
	global_load_dwordx4 v[32:35], v21, s[8:9] offset:0
	v_mfma_f32_16x16x32_bf16 v[136:139], v[96:99], v[88:91], v[136:139]
	v_mfma_f32_16x16x32_bf16 v[140:143], v[96:99], v[92:95], v[140:143]
	global_load_dwordx4 v[36:39], v21, s[8:9] offset:16
	v_mfma_f32_16x16x32_bf16 v[144:147], v[100:103], v[80:83], v[144:147]
	v_mfma_f32_16x16x32_bf16 v[148:151], v[100:103], v[84:87], v[148:151]
	global_load_dwordx4 v[40:43], v21, s[8:9] offset:32
	v_mfma_f32_16x16x32_bf16 v[152:155], v[100:103], v[88:91], v[152:155]
	v_mfma_f32_16x16x32_bf16 v[156:159], v[100:103], v[92:95], v[156:159]
	global_load_dwordx4 v[44:47], v21, s[8:9] offset:48
	v_mfma_f32_16x16x32_bf16 v[160:163], v[104:107], v[80:83], v[160:163]
	v_mfma_f32_16x16x32_bf16 v[164:167], v[104:107], v[84:87], v[164:167]
	global_load_dwordx4 v[48:51], v21, s[8:9] offset:1024
	v_mfma_f32_16x16x32_bf16 v[168:171], v[104:107], v[88:91], v[168:171]
	v_mfma_f32_16x16x32_bf16 v[172:175], v[104:107], v[92:95], v[172:175]
	global_load_dwordx4 v[52:55], v21, s[8:9] offset:1040
	v_mfma_f32_16x16x32_bf16 v[176:179], v[108:111], v[80:83], v[176:179]
	v_mfma_f32_16x16x32_bf16 v[180:183], v[108:111], v[84:87], v[180:183]
	global_load_dwordx4 v[56:59], v21, s[8:9] offset:1056
	v_mfma_f32_16x16x32_bf16 v[184:187], v[108:111], v[88:91], v[184:187]
	v_mfma_f32_16x16x32_bf16 v[188:191], v[108:111], v[92:95], v[188:191]
	global_load_dwordx4 v[60:63], v21, s[8:9] offset:1072
	v_mfma_f32_16x16x32_bf16 v[192:195], v[112:115], v[80:83], v[192:195]
	v_mfma_f32_16x16x32_bf16 v[196:199], v[112:115], v[84:87], v[196:199]
	global_load_dwordx4 v[64:67], v21, s[8:9] offset:2048
	v_mfma_f32_16x16x32_bf16 v[200:203], v[112:115], v[88:91], v[200:203]
	v_mfma_f32_16x16x32_bf16 v[204:207], v[112:115], v[92:95], v[204:207]
	global_load_dwordx4 v[68:71], v21, s[8:9] offset:2064
	v_mfma_f32_16x16x32_bf16 v[208:211], v[116:119], v[80:83], v[208:211]
	v_mfma_f32_16x16x32_bf16 v[212:215], v[116:119], v[84:87], v[212:215]
	global_load_dwordx4 v[72:75], v21, s[8:9] offset:2080
	v_mfma_f32_16x16x32_bf16 v[216:219], v[116:119], v[88:91], v[216:219]
	v_mfma_f32_16x16x32_bf16 v[220:223], v[116:119], v[92:95], v[220:223]
	global_load_dwordx4 v[76:79], v21, s[8:9] offset:2096
	v_mfma_f32_16x16x32_bf16 v[224:227], v[120:123], v[80:83], v[224:227]
	v_mfma_f32_16x16x32_bf16 v[228:231], v[120:123], v[84:87], v[228:231]
	v_mfma_f32_16x16x32_bf16 v[232:235], v[120:123], v[88:91], v[232:235]
	v_mfma_f32_16x16x32_bf16 v[236:239], v[120:123], v[92:95], v[236:239]
	v_mfma_f32_16x16x32_bf16 v[240:243], v[124:127], v[80:83], v[240:243]
	v_mfma_f32_16x16x32_bf16 v[244:247], v[124:127], v[84:87], v[244:247]
	v_mfma_f32_16x16x32_bf16 v[248:251], v[124:127], v[88:91], v[248:251]
	v_mfma_f32_16x16x32_bf16 v[252:255], v[124:127], v[92:95], v[252:255]
	global_load_dwordx4 v[80:83], v21, s[8:9] offset:3072
	global_load_dwordx4 v[84:87], v21, s[8:9] offset:3088
	global_load_dwordx4 v[88:91], v21, s[8:9] offset:3104
	global_load_dwordx4 v[92:95], v21, s[8:9] offset:3120
	v_mov_b32_e32 v31, 0x358637bd
	s_waitcnt vmcnt(0)
	v_add_f32_e32 v32, v32, v33
	v_add_f32_e32 v34, v34, v35
	v_add_f32_e32 v36, v36, v37
	v_add_f32_e32 v38, v38, v39
	v_add_f32_e32 v40, v40, v41
	v_add_f32_e32 v42, v42, v43
	v_add_f32_e32 v44, v44, v45
	v_add_f32_e32 v46, v46, v47
	v_add_f32_e32 v32, v32, v34
	v_add_f32_e32 v36, v36, v38
	v_add_f32_e32 v40, v40, v42
	v_add_f32_e32 v44, v44, v46
	v_add_f32_e32 v32, v32, v36
	v_add_f32_e32 v40, v40, v44
	s_nop 0
	v_add_f32_e32 v32, v32, v40
	v_add_f32_e32 v48, v48, v49
	v_add_f32_e32 v50, v50, v51
	v_add_f32_e32 v52, v52, v53
	v_add_f32_e32 v54, v54, v55
	v_add_f32_e32 v56, v56, v57
	v_add_f32_e32 v58, v58, v59
	v_add_f32_e32 v60, v60, v61
	v_add_f32_e32 v62, v62, v63
	v_add_f32_e32 v48, v48, v50
	v_add_f32_e32 v52, v52, v54
	v_add_f32_e32 v56, v56, v58
	v_add_f32_e32 v60, v60, v62
	v_add_f32_e32 v48, v48, v52
	v_add_f32_e32 v56, v56, v60
	s_nop 0
	v_add_f32_e32 v48, v48, v56
	v_add_f32_e32 v64, v64, v65
	v_add_f32_e32 v66, v66, v67
	v_add_f32_e32 v68, v68, v69
	v_add_f32_e32 v70, v70, v71
	v_add_f32_e32 v72, v72, v73
	v_add_f32_e32 v74, v74, v75
	v_add_f32_e32 v76, v76, v77
	v_add_f32_e32 v78, v78, v79
	v_add_f32_e32 v64, v64, v66
	v_add_f32_e32 v68, v68, v70
	v_add_f32_e32 v72, v72, v74
	v_add_f32_e32 v76, v76, v78
	v_add_f32_e32 v64, v64, v68
	v_add_f32_e32 v72, v72, v76
	s_nop 0
	v_add_f32_e32 v64, v64, v72
	v_add_f32_e32 v80, v80, v81
	v_add_f32_e32 v82, v82, v83
	v_add_f32_e32 v84, v84, v85
	v_add_f32_e32 v86, v86, v87
	v_add_f32_e32 v88, v88, v89
	v_add_f32_e32 v90, v90, v91
	v_add_f32_e32 v92, v92, v93
	v_add_f32_e32 v94, v94, v95
	v_add_f32_e32 v80, v80, v82
	v_add_f32_e32 v84, v84, v86
	v_add_f32_e32 v88, v88, v90
	v_add_f32_e32 v92, v92, v94
	v_add_f32_e32 v80, v80, v84
	v_add_f32_e32 v88, v88, v92
	s_nop 0
	v_add_f32_e32 v80, v80, v88
	v_fmamk_f32 v20, v32, 0x3aaaaaab, v31
	v_fmamk_f32 v22, v48, 0x3aaaaaab, v31
	v_fmamk_f32 v24, v64, 0x3aaaaaab, v31
	v_fmamk_f32 v26, v80, 0x3aaaaaab, v31
	v_rsq_f32_e32 v20, v20
	v_rsq_f32_e32 v22, v22
	v_rsq_f32_e32 v24, v24
	v_rsq_f32_e32 v26, v26
	s_nop 0
	v_pk_mul_f32 v[128:129], v[128:129], v[20:21] op_sel_hi:[1,0]
	v_pk_mul_f32 v[130:131], v[130:131], v[20:21] op_sel_hi:[1,0]
	v_pk_mul_f32 v[144:145], v[144:145], v[20:21] op_sel_hi:[1,0]
	v_pk_mul_f32 v[146:147], v[146:147], v[20:21] op_sel_hi:[1,0]
	v_mul_f32_e32 v32, 0x3dd2d3e8, v128
	v_mul_f32_e32 v33, 0x3dd2d3e8, v129
	v_mul_f32_e32 v34, 0x3dd2d3e8, v130
	v_mul_f32_e32 v35, 0x3dd2d3e8, v131
	v_mul_f32_e32 v36, 0x3dd2d3e8, v144
	v_mul_f32_e32 v37, 0x3dd2d3e8, v145
	v_mul_f32_e32 v38, 0x3dd2d3e8, v146
	v_mul_f32_e32 v39, 0x3dd2d3e8, v147
	v_fma_f32 v32, -v128, v32, s24
	v_fma_f32 v33, -v129, v33, s24
	v_fma_f32 v34, -v130, v34, s24
	v_fma_f32 v35, -v131, v35, s24
	v_fma_f32 v36, -v144, v36, s24
	v_fma_f32 v37, -v145, v37, s24
	v_fma_f32 v38, -v146, v38, s24
	v_fma_f32 v39, -v147, v39, s24
	v_mul_f32_e32 v32, v128, v32
	v_mul_f32_e32 v33, v129, v33
	v_mul_f32_e32 v34, v130, v34
	v_mul_f32_e32 v35, v131, v35
	v_mul_f32_e32 v36, v144, v36
	v_mul_f32_e32 v37, v145, v37
	v_mul_f32_e32 v38, v146, v38
	v_mul_f32_e32 v39, v147, v39
	v_exp_f32_e32 v32, v32
	v_exp_f32_e32 v33, v33
	v_exp_f32_e32 v34, v34
	v_exp_f32_e32 v35, v35
	v_exp_f32_e32 v36, v36
	v_exp_f32_e32 v37, v37
	v_exp_f32_e32 v38, v38
	v_exp_f32_e32 v39, v39
	v_add_f32_e32 v32, 1.0, v32
	v_add_f32_e32 v33, 1.0, v33
	v_add_f32_e32 v34, 1.0, v34
	v_add_f32_e32 v35, 1.0, v35
	v_add_f32_e32 v36, 1.0, v36
	v_add_f32_e32 v37, 1.0, v37
	v_add_f32_e32 v38, 1.0, v38
	v_add_f32_e32 v39, 1.0, v39
	v_rcp_f32_e32 v32, v32
	v_rcp_f32_e32 v33, v33
	v_rcp_f32_e32 v34, v34
	v_rcp_f32_e32 v35, v35
	v_rcp_f32_e32 v36, v36
	v_rcp_f32_e32 v37, v37
	v_rcp_f32_e32 v38, v38
	v_rcp_f32_e32 v39, v39
	s_nop 0
	v_pk_mul_f32 v[128:129], v[128:129], v[32:33]
	v_pk_mul_f32 v[130:131], v[130:131], v[34:35]
	v_pk_mul_f32 v[144:145], v[144:145], v[36:37]
	v_pk_mul_f32 v[146:147], v[146:147], v[38:39]
	v_cvt_pk_bf16_f32 v64, v128, v129
	v_cvt_pk_bf16_f32 v65, v130, v131
	v_cvt_pk_bf16_f32 v66, v144, v145
	v_cvt_pk_bf16_f32 v67, v146, v147
	global_store_dwordx2 v16, v[64:65], s[10:11]
	global_store_dwordx2 v16, v[66:67], s[10:11] offset:32
	v_pk_mul_f32 v[160:161], v[160:161], v[20:21] op_sel_hi:[1,0]
	v_pk_mul_f32 v[162:163], v[162:163], v[20:21] op_sel_hi:[1,0]
	v_pk_mul_f32 v[176:177], v[176:177], v[20:21] op_sel_hi:[1,0]
	v_pk_mul_f32 v[178:179], v[178:179], v[20:21] op_sel_hi:[1,0]
	v_mul_f32_e32 v48, 0x3dd2d3e8, v160
	v_mul_f32_e32 v49, 0x3dd2d3e8, v161
	v_mul_f32_e32 v50, 0x3dd2d3e8, v162
	v_mul_f32_e32 v51, 0x3dd2d3e8, v163
	v_mul_f32_e32 v52, 0x3dd2d3e8, v176
	v_mul_f32_e32 v53, 0x3dd2d3e8, v177
	v_mul_f32_e32 v54, 0x3dd2d3e8, v178
	v_mul_f32_e32 v55, 0x3dd2d3e8, v179
	v_fma_f32 v48, -v160, v48, s24
	v_fma_f32 v49, -v161, v49, s24
	v_fma_f32 v50, -v162, v50, s24
	v_fma_f32 v51, -v163, v51, s24
	v_fma_f32 v52, -v176, v52, s24
	v_fma_f32 v53, -v177, v53, s24
	v_fma_f32 v54, -v178, v54, s24
	v_fma_f32 v55, -v179, v55, s24
	v_mul_f32_e32 v48, v160, v48
	v_mul_f32_e32 v49, v161, v49
	v_mul_f32_e32 v50, v162, v50
	v_mul_f32_e32 v51, v163, v51
	v_mul_f32_e32 v52, v176, v52
	v_mul_f32_e32 v53, v177, v53
	v_mul_f32_e32 v54, v178, v54
	v_mul_f32_e32 v55, v179, v55
	v_exp_f32_e32 v48, v48
	v_exp_f32_e32 v49, v49
	v_exp_f32_e32 v50, v50
	v_exp_f32_e32 v51, v51
	v_exp_f32_e32 v52, v52
	v_exp_f32_e32 v53, v53
	v_exp_f32_e32 v54, v54
	v_exp_f32_e32 v55, v55
	v_add_f32_e32 v48, 1.0, v48
	v_add_f32_e32 v49, 1.0, v49
	v_add_f32_e32 v50, 1.0, v50
	v_add_f32_e32 v51, 1.0, v51
	v_add_f32_e32 v52, 1.0, v52
	v_add_f32_e32 v53, 1.0, v53
	v_add_f32_e32 v54, 1.0, v54
	v_add_f32_e32 v55, 1.0, v55
	v_rcp_f32_e32 v48, v48
	v_rcp_f32_e32 v49, v49
	v_rcp_f32_e32 v50, v50
	v_rcp_f32_e32 v51, v51
	v_rcp_f32_e32 v52, v52
	v_rcp_f32_e32 v53, v53
	v_rcp_f32_e32 v54, v54
	v_rcp_f32_e32 v55, v55
	s_nop 0
	v_pk_mul_f32 v[160:161], v[160:161], v[48:49]
	v_pk_mul_f32 v[162:163], v[162:163], v[50:51]
	v_pk_mul_f32 v[176:177], v[176:177], v[52:53]
	v_pk_mul_f32 v[178:179], v[178:179], v[54:55]
	v_cvt_pk_bf16_f32 v68, v160, v161
	v_cvt_pk_bf16_f32 v69, v162, v163
	v_cvt_pk_bf16_f32 v70, v176, v177
	v_cvt_pk_bf16_f32 v71, v178, v179
	global_store_dwordx2 v16, v[68:69], s[10:11] offset:64
	global_store_dwordx2 v16, v[70:71], s[10:11] offset:96
	v_pk_mul_f32 v[192:193], v[192:193], v[20:21] op_sel_hi:[1,0]
	v_pk_mul_f32 v[194:195], v[194:195], v[20:21] op_sel_hi:[1,0]
	v_pk_mul_f32 v[208:209], v[208:209], v[20:21] op_sel_hi:[1,0]
	v_pk_mul_f32 v[210:211], v[210:211], v[20:21] op_sel_hi:[1,0]
	v_mul_f32_e32 v32, 0x3dd2d3e8, v192
	v_mul_f32_e32 v33, 0x3dd2d3e8, v193
	v_mul_f32_e32 v34, 0x3dd2d3e8, v194
	v_mul_f32_e32 v35, 0x3dd2d3e8, v195
	v_mul_f32_e32 v36, 0x3dd2d3e8, v208
	v_mul_f32_e32 v37, 0x3dd2d3e8, v209
	v_mul_f32_e32 v38, 0x3dd2d3e8, v210
	v_mul_f32_e32 v39, 0x3dd2d3e8, v211
	v_fma_f32 v32, -v192, v32, s24
	v_fma_f32 v33, -v193, v33, s24
	v_fma_f32 v34, -v194, v34, s24
	v_fma_f32 v35, -v195, v35, s24
	v_fma_f32 v36, -v208, v36, s24
	v_fma_f32 v37, -v209, v37, s24
	v_fma_f32 v38, -v210, v38, s24
	v_fma_f32 v39, -v211, v39, s24
	v_mul_f32_e32 v32, v192, v32
	v_mul_f32_e32 v33, v193, v33
	v_mul_f32_e32 v34, v194, v34
	v_mul_f32_e32 v35, v195, v35
	v_mul_f32_e32 v36, v208, v36
	v_mul_f32_e32 v37, v209, v37
	v_mul_f32_e32 v38, v210, v38
	v_mul_f32_e32 v39, v211, v39
	v_exp_f32_e32 v32, v32
	v_exp_f32_e32 v33, v33
	v_exp_f32_e32 v34, v34
	v_exp_f32_e32 v35, v35
	v_exp_f32_e32 v36, v36
	v_exp_f32_e32 v37, v37
	v_exp_f32_e32 v38, v38
	v_exp_f32_e32 v39, v39
	v_add_f32_e32 v32, 1.0, v32
	v_add_f32_e32 v33, 1.0, v33
	v_add_f32_e32 v34, 1.0, v34
	v_add_f32_e32 v35, 1.0, v35
	v_add_f32_e32 v36, 1.0, v36
	v_add_f32_e32 v37, 1.0, v37
	v_add_f32_e32 v38, 1.0, v38
	v_add_f32_e32 v39, 1.0, v39
	v_rcp_f32_e32 v32, v32
	v_rcp_f32_e32 v33, v33
	v_rcp_f32_e32 v34, v34
	v_rcp_f32_e32 v35, v35
	v_rcp_f32_e32 v36, v36
	v_rcp_f32_e32 v37, v37
	v_rcp_f32_e32 v38, v38
	v_rcp_f32_e32 v39, v39
	s_nop 0
	v_pk_mul_f32 v[192:193], v[192:193], v[32:33]
	v_pk_mul_f32 v[194:195], v[194:195], v[34:35]
	v_pk_mul_f32 v[208:209], v[208:209], v[36:37]
	v_pk_mul_f32 v[210:211], v[210:211], v[38:39]
	v_cvt_pk_bf16_f32 v64, v192, v193
	v_cvt_pk_bf16_f32 v65, v194, v195
	v_cvt_pk_bf16_f32 v66, v208, v209
	v_cvt_pk_bf16_f32 v67, v210, v211
	global_store_dwordx2 v16, v[64:65], s[10:11] offset:128
	global_store_dwordx2 v16, v[66:67], s[10:11] offset:160
	v_pk_mul_f32 v[224:225], v[224:225], v[20:21] op_sel_hi:[1,0]
	v_pk_mul_f32 v[226:227], v[226:227], v[20:21] op_sel_hi:[1,0]
	v_pk_mul_f32 v[240:241], v[240:241], v[20:21] op_sel_hi:[1,0]
	v_pk_mul_f32 v[242:243], v[242:243], v[20:21] op_sel_hi:[1,0]
	v_mul_f32_e32 v48, 0x3dd2d3e8, v224
	v_mul_f32_e32 v49, 0x3dd2d3e8, v225
	v_mul_f32_e32 v50, 0x3dd2d3e8, v226
	v_mul_f32_e32 v51, 0x3dd2d3e8, v227
	v_mul_f32_e32 v52, 0x3dd2d3e8, v240
	v_mul_f32_e32 v53, 0x3dd2d3e8, v241
	v_mul_f32_e32 v54, 0x3dd2d3e8, v242
	v_mul_f32_e32 v55, 0x3dd2d3e8, v243
	v_fma_f32 v48, -v224, v48, s24
	v_fma_f32 v49, -v225, v49, s24
	v_fma_f32 v50, -v226, v50, s24
	v_fma_f32 v51, -v227, v51, s24
	v_fma_f32 v52, -v240, v52, s24
	v_fma_f32 v53, -v241, v53, s24
	v_fma_f32 v54, -v242, v54, s24
	v_fma_f32 v55, -v243, v55, s24
	v_mul_f32_e32 v48, v224, v48
	v_mul_f32_e32 v49, v225, v49
	v_mul_f32_e32 v50, v226, v50
	v_mul_f32_e32 v51, v227, v51
	v_mul_f32_e32 v52, v240, v52
	v_mul_f32_e32 v53, v241, v53
	v_mul_f32_e32 v54, v242, v54
	v_mul_f32_e32 v55, v243, v55
	v_exp_f32_e32 v48, v48
	v_exp_f32_e32 v49, v49
	v_exp_f32_e32 v50, v50
	v_exp_f32_e32 v51, v51
	v_exp_f32_e32 v52, v52
	v_exp_f32_e32 v53, v53
	v_exp_f32_e32 v54, v54
	v_exp_f32_e32 v55, v55
	v_add_f32_e32 v48, 1.0, v48
	v_add_f32_e32 v49, 1.0, v49
	v_add_f32_e32 v50, 1.0, v50
	v_add_f32_e32 v51, 1.0, v51
	v_add_f32_e32 v52, 1.0, v52
	v_add_f32_e32 v53, 1.0, v53
	v_add_f32_e32 v54, 1.0, v54
	v_add_f32_e32 v55, 1.0, v55
	v_rcp_f32_e32 v48, v48
	v_rcp_f32_e32 v49, v49
	v_rcp_f32_e32 v50, v50
	v_rcp_f32_e32 v51, v51
	v_rcp_f32_e32 v52, v52
	v_rcp_f32_e32 v53, v53
	v_rcp_f32_e32 v54, v54
	v_rcp_f32_e32 v55, v55
	s_nop 0
	v_pk_mul_f32 v[224:225], v[224:225], v[48:49]
	v_pk_mul_f32 v[226:227], v[226:227], v[50:51]
	v_pk_mul_f32 v[240:241], v[240:241], v[52:53]
	v_pk_mul_f32 v[242:243], v[242:243], v[54:55]
	v_cvt_pk_bf16_f32 v68, v224, v225
	v_cvt_pk_bf16_f32 v69, v226, v227
	v_cvt_pk_bf16_f32 v70, v240, v241
	v_cvt_pk_bf16_f32 v71, v242, v243
	global_store_dwordx2 v16, v[68:69], s[10:11] offset:192
	global_store_dwordx2 v16, v[70:71], s[10:11] offset:224
	v_pk_mul_f32 v[132:133], v[132:133], v[22:23] op_sel_hi:[1,0]
	v_pk_mul_f32 v[134:135], v[134:135], v[22:23] op_sel_hi:[1,0]
	v_pk_mul_f32 v[148:149], v[148:149], v[22:23] op_sel_hi:[1,0]
	v_pk_mul_f32 v[150:151], v[150:151], v[22:23] op_sel_hi:[1,0]
	v_mul_f32_e32 v32, 0x3dd2d3e8, v132
	v_mul_f32_e32 v33, 0x3dd2d3e8, v133
	v_mul_f32_e32 v34, 0x3dd2d3e8, v134
	v_mul_f32_e32 v35, 0x3dd2d3e8, v135
	v_mul_f32_e32 v36, 0x3dd2d3e8, v148
	v_mul_f32_e32 v37, 0x3dd2d3e8, v149
	v_mul_f32_e32 v38, 0x3dd2d3e8, v150
	v_mul_f32_e32 v39, 0x3dd2d3e8, v151
	v_fma_f32 v32, -v132, v32, s24
	v_fma_f32 v33, -v133, v33, s24
	v_fma_f32 v34, -v134, v34, s24
	v_fma_f32 v35, -v135, v35, s24
	v_fma_f32 v36, -v148, v36, s24
	v_fma_f32 v37, -v149, v37, s24
	v_fma_f32 v38, -v150, v38, s24
	v_fma_f32 v39, -v151, v39, s24
	v_mul_f32_e32 v32, v132, v32
	v_mul_f32_e32 v33, v133, v33
	v_mul_f32_e32 v34, v134, v34
	v_mul_f32_e32 v35, v135, v35
	v_mul_f32_e32 v36, v148, v36
	v_mul_f32_e32 v37, v149, v37
	v_mul_f32_e32 v38, v150, v38
	v_mul_f32_e32 v39, v151, v39
	v_exp_f32_e32 v32, v32
	v_exp_f32_e32 v33, v33
	v_exp_f32_e32 v34, v34
	v_exp_f32_e32 v35, v35
	v_exp_f32_e32 v36, v36
	v_exp_f32_e32 v37, v37
	v_exp_f32_e32 v38, v38
	v_exp_f32_e32 v39, v39
	v_add_f32_e32 v32, 1.0, v32
	v_add_f32_e32 v33, 1.0, v33
	v_add_f32_e32 v34, 1.0, v34
	v_add_f32_e32 v35, 1.0, v35
	v_add_f32_e32 v36, 1.0, v36
	v_add_f32_e32 v37, 1.0, v37
	v_add_f32_e32 v38, 1.0, v38
	v_add_f32_e32 v39, 1.0, v39
	v_rcp_f32_e32 v32, v32
	v_rcp_f32_e32 v33, v33
	v_rcp_f32_e32 v34, v34
	v_rcp_f32_e32 v35, v35
	v_rcp_f32_e32 v36, v36
	v_rcp_f32_e32 v37, v37
	v_rcp_f32_e32 v38, v38
	v_rcp_f32_e32 v39, v39
	s_nop 0
	v_pk_mul_f32 v[132:133], v[132:133], v[32:33]
	v_pk_mul_f32 v[134:135], v[134:135], v[34:35]
	v_pk_mul_f32 v[148:149], v[148:149], v[36:37]
	v_pk_mul_f32 v[150:151], v[150:151], v[38:39]
	v_cvt_pk_bf16_f32 v64, v132, v133
	v_cvt_pk_bf16_f32 v65, v134, v135
	v_cvt_pk_bf16_f32 v66, v148, v149
	v_cvt_pk_bf16_f32 v67, v150, v151
	global_store_dwordx2 v17, v[64:65], s[10:11]
	global_store_dwordx2 v17, v[66:67], s[10:11] offset:32
	v_pk_mul_f32 v[164:165], v[164:165], v[22:23] op_sel_hi:[1,0]
	v_pk_mul_f32 v[166:167], v[166:167], v[22:23] op_sel_hi:[1,0]
	v_pk_mul_f32 v[180:181], v[180:181], v[22:23] op_sel_hi:[1,0]
	v_pk_mul_f32 v[182:183], v[182:183], v[22:23] op_sel_hi:[1,0]
	v_mul_f32_e32 v48, 0x3dd2d3e8, v164
	v_mul_f32_e32 v49, 0x3dd2d3e8, v165
	v_mul_f32_e32 v50, 0x3dd2d3e8, v166
	v_mul_f32_e32 v51, 0x3dd2d3e8, v167
	v_mul_f32_e32 v52, 0x3dd2d3e8, v180
	v_mul_f32_e32 v53, 0x3dd2d3e8, v181
	v_mul_f32_e32 v54, 0x3dd2d3e8, v182
	v_mul_f32_e32 v55, 0x3dd2d3e8, v183
	v_fma_f32 v48, -v164, v48, s24
	v_fma_f32 v49, -v165, v49, s24
	v_fma_f32 v50, -v166, v50, s24
	v_fma_f32 v51, -v167, v51, s24
	v_fma_f32 v52, -v180, v52, s24
	v_fma_f32 v53, -v181, v53, s24
	v_fma_f32 v54, -v182, v54, s24
	v_fma_f32 v55, -v183, v55, s24
	v_mul_f32_e32 v48, v164, v48
	v_mul_f32_e32 v49, v165, v49
	v_mul_f32_e32 v50, v166, v50
	v_mul_f32_e32 v51, v167, v51
	v_mul_f32_e32 v52, v180, v52
	v_mul_f32_e32 v53, v181, v53
	v_mul_f32_e32 v54, v182, v54
	v_mul_f32_e32 v55, v183, v55
	v_exp_f32_e32 v48, v48
	v_exp_f32_e32 v49, v49
	v_exp_f32_e32 v50, v50
	v_exp_f32_e32 v51, v51
	v_exp_f32_e32 v52, v52
	v_exp_f32_e32 v53, v53
	v_exp_f32_e32 v54, v54
	v_exp_f32_e32 v55, v55
	v_add_f32_e32 v48, 1.0, v48
	v_add_f32_e32 v49, 1.0, v49
	v_add_f32_e32 v50, 1.0, v50
	v_add_f32_e32 v51, 1.0, v51
	v_add_f32_e32 v52, 1.0, v52
	v_add_f32_e32 v53, 1.0, v53
	v_add_f32_e32 v54, 1.0, v54
	v_add_f32_e32 v55, 1.0, v55
	v_rcp_f32_e32 v48, v48
	v_rcp_f32_e32 v49, v49
	v_rcp_f32_e32 v50, v50
	v_rcp_f32_e32 v51, v51
	v_rcp_f32_e32 v52, v52
	v_rcp_f32_e32 v53, v53
	v_rcp_f32_e32 v54, v54
	v_rcp_f32_e32 v55, v55
	s_nop 0
	v_pk_mul_f32 v[164:165], v[164:165], v[48:49]
	v_pk_mul_f32 v[166:167], v[166:167], v[50:51]
	v_pk_mul_f32 v[180:181], v[180:181], v[52:53]
	v_pk_mul_f32 v[182:183], v[182:183], v[54:55]
	v_cvt_pk_bf16_f32 v68, v164, v165
	v_cvt_pk_bf16_f32 v69, v166, v167
	v_cvt_pk_bf16_f32 v70, v180, v181
	v_cvt_pk_bf16_f32 v71, v182, v183
	global_store_dwordx2 v17, v[68:69], s[10:11] offset:64
	global_store_dwordx2 v17, v[70:71], s[10:11] offset:96
	v_pk_mul_f32 v[196:197], v[196:197], v[22:23] op_sel_hi:[1,0]
	v_pk_mul_f32 v[198:199], v[198:199], v[22:23] op_sel_hi:[1,0]
	v_pk_mul_f32 v[212:213], v[212:213], v[22:23] op_sel_hi:[1,0]
	v_pk_mul_f32 v[214:215], v[214:215], v[22:23] op_sel_hi:[1,0]
	v_mul_f32_e32 v32, 0x3dd2d3e8, v196
	v_mul_f32_e32 v33, 0x3dd2d3e8, v197
	v_mul_f32_e32 v34, 0x3dd2d3e8, v198
	v_mul_f32_e32 v35, 0x3dd2d3e8, v199
	v_mul_f32_e32 v36, 0x3dd2d3e8, v212
	v_mul_f32_e32 v37, 0x3dd2d3e8, v213
	v_mul_f32_e32 v38, 0x3dd2d3e8, v214
	v_mul_f32_e32 v39, 0x3dd2d3e8, v215
	v_fma_f32 v32, -v196, v32, s24
	v_fma_f32 v33, -v197, v33, s24
	v_fma_f32 v34, -v198, v34, s24
	v_fma_f32 v35, -v199, v35, s24
	v_fma_f32 v36, -v212, v36, s24
	v_fma_f32 v37, -v213, v37, s24
	v_fma_f32 v38, -v214, v38, s24
	v_fma_f32 v39, -v215, v39, s24
	v_mul_f32_e32 v32, v196, v32
	v_mul_f32_e32 v33, v197, v33
	v_mul_f32_e32 v34, v198, v34
	v_mul_f32_e32 v35, v199, v35
	v_mul_f32_e32 v36, v212, v36
	v_mul_f32_e32 v37, v213, v37
	v_mul_f32_e32 v38, v214, v38
	v_mul_f32_e32 v39, v215, v39
	v_exp_f32_e32 v32, v32
	v_exp_f32_e32 v33, v33
	v_exp_f32_e32 v34, v34
	v_exp_f32_e32 v35, v35
	v_exp_f32_e32 v36, v36
	v_exp_f32_e32 v37, v37
	v_exp_f32_e32 v38, v38
	v_exp_f32_e32 v39, v39
	v_add_f32_e32 v32, 1.0, v32
	v_add_f32_e32 v33, 1.0, v33
	v_add_f32_e32 v34, 1.0, v34
	v_add_f32_e32 v35, 1.0, v35
	v_add_f32_e32 v36, 1.0, v36
	v_add_f32_e32 v37, 1.0, v37
	v_add_f32_e32 v38, 1.0, v38
	v_add_f32_e32 v39, 1.0, v39
	v_rcp_f32_e32 v32, v32
	v_rcp_f32_e32 v33, v33
	v_rcp_f32_e32 v34, v34
	v_rcp_f32_e32 v35, v35
	v_rcp_f32_e32 v36, v36
	v_rcp_f32_e32 v37, v37
	v_rcp_f32_e32 v38, v38
	v_rcp_f32_e32 v39, v39
	s_nop 0
	v_pk_mul_f32 v[196:197], v[196:197], v[32:33]
	v_pk_mul_f32 v[198:199], v[198:199], v[34:35]
	v_pk_mul_f32 v[212:213], v[212:213], v[36:37]
	v_pk_mul_f32 v[214:215], v[214:215], v[38:39]
	v_cvt_pk_bf16_f32 v64, v196, v197
	v_cvt_pk_bf16_f32 v65, v198, v199
	v_cvt_pk_bf16_f32 v66, v212, v213
	v_cvt_pk_bf16_f32 v67, v214, v215
	global_store_dwordx2 v17, v[64:65], s[10:11] offset:128
	global_store_dwordx2 v17, v[66:67], s[10:11] offset:160
	v_pk_mul_f32 v[228:229], v[228:229], v[22:23] op_sel_hi:[1,0]
	v_pk_mul_f32 v[230:231], v[230:231], v[22:23] op_sel_hi:[1,0]
	v_pk_mul_f32 v[244:245], v[244:245], v[22:23] op_sel_hi:[1,0]
	v_pk_mul_f32 v[246:247], v[246:247], v[22:23] op_sel_hi:[1,0]
	v_mul_f32_e32 v48, 0x3dd2d3e8, v228
	v_mul_f32_e32 v49, 0x3dd2d3e8, v229
	v_mul_f32_e32 v50, 0x3dd2d3e8, v230
	v_mul_f32_e32 v51, 0x3dd2d3e8, v231
	v_mul_f32_e32 v52, 0x3dd2d3e8, v244
	v_mul_f32_e32 v53, 0x3dd2d3e8, v245
	v_mul_f32_e32 v54, 0x3dd2d3e8, v246
	v_mul_f32_e32 v55, 0x3dd2d3e8, v247
	v_fma_f32 v48, -v228, v48, s24
	v_fma_f32 v49, -v229, v49, s24
	v_fma_f32 v50, -v230, v50, s24
	v_fma_f32 v51, -v231, v51, s24
	v_fma_f32 v52, -v244, v52, s24
	v_fma_f32 v53, -v245, v53, s24
	v_fma_f32 v54, -v246, v54, s24
	v_fma_f32 v55, -v247, v55, s24
	v_mul_f32_e32 v48, v228, v48
	v_mul_f32_e32 v49, v229, v49
	v_mul_f32_e32 v50, v230, v50
	v_mul_f32_e32 v51, v231, v51
	v_mul_f32_e32 v52, v244, v52
	v_mul_f32_e32 v53, v245, v53
	v_mul_f32_e32 v54, v246, v54
	v_mul_f32_e32 v55, v247, v55
	v_exp_f32_e32 v48, v48
	v_exp_f32_e32 v49, v49
	v_exp_f32_e32 v50, v50
	v_exp_f32_e32 v51, v51
	v_exp_f32_e32 v52, v52
	v_exp_f32_e32 v53, v53
	v_exp_f32_e32 v54, v54
	v_exp_f32_e32 v55, v55
	v_add_f32_e32 v48, 1.0, v48
	v_add_f32_e32 v49, 1.0, v49
	v_add_f32_e32 v50, 1.0, v50
	v_add_f32_e32 v51, 1.0, v51
	v_add_f32_e32 v52, 1.0, v52
	v_add_f32_e32 v53, 1.0, v53
	v_add_f32_e32 v54, 1.0, v54
	v_add_f32_e32 v55, 1.0, v55
	v_rcp_f32_e32 v48, v48
	v_rcp_f32_e32 v49, v49
	v_rcp_f32_e32 v50, v50
	v_rcp_f32_e32 v51, v51
	v_rcp_f32_e32 v52, v52
	v_rcp_f32_e32 v53, v53
	v_rcp_f32_e32 v54, v54
	v_rcp_f32_e32 v55, v55
	s_nop 0
	v_pk_mul_f32 v[228:229], v[228:229], v[48:49]
	v_pk_mul_f32 v[230:231], v[230:231], v[50:51]
	v_pk_mul_f32 v[244:245], v[244:245], v[52:53]
	v_pk_mul_f32 v[246:247], v[246:247], v[54:55]
	v_cvt_pk_bf16_f32 v68, v228, v229
	v_cvt_pk_bf16_f32 v69, v230, v231
	v_cvt_pk_bf16_f32 v70, v244, v245
	v_cvt_pk_bf16_f32 v71, v246, v247
	global_store_dwordx2 v17, v[68:69], s[10:11] offset:192
	global_store_dwordx2 v17, v[70:71], s[10:11] offset:224
	v_pk_mul_f32 v[136:137], v[136:137], v[24:25] op_sel_hi:[1,0]
	v_pk_mul_f32 v[138:139], v[138:139], v[24:25] op_sel_hi:[1,0]
	v_pk_mul_f32 v[152:153], v[152:153], v[24:25] op_sel_hi:[1,0]
	v_pk_mul_f32 v[154:155], v[154:155], v[24:25] op_sel_hi:[1,0]
	v_mul_f32_e32 v32, 0x3dd2d3e8, v136
	v_mul_f32_e32 v33, 0x3dd2d3e8, v137
	v_mul_f32_e32 v34, 0x3dd2d3e8, v138
	v_mul_f32_e32 v35, 0x3dd2d3e8, v139
	v_mul_f32_e32 v36, 0x3dd2d3e8, v152
	v_mul_f32_e32 v37, 0x3dd2d3e8, v153
	v_mul_f32_e32 v38, 0x3dd2d3e8, v154
	v_mul_f32_e32 v39, 0x3dd2d3e8, v155
	v_fma_f32 v32, -v136, v32, s24
	v_fma_f32 v33, -v137, v33, s24
	v_fma_f32 v34, -v138, v34, s24
	v_fma_f32 v35, -v139, v35, s24
	v_fma_f32 v36, -v152, v36, s24
	v_fma_f32 v37, -v153, v37, s24
	v_fma_f32 v38, -v154, v38, s24
	v_fma_f32 v39, -v155, v39, s24
	v_mul_f32_e32 v32, v136, v32
	v_mul_f32_e32 v33, v137, v33
	v_mul_f32_e32 v34, v138, v34
	v_mul_f32_e32 v35, v139, v35
	v_mul_f32_e32 v36, v152, v36
	v_mul_f32_e32 v37, v153, v37
	v_mul_f32_e32 v38, v154, v38
	v_mul_f32_e32 v39, v155, v39
	v_exp_f32_e32 v32, v32
	v_exp_f32_e32 v33, v33
	v_exp_f32_e32 v34, v34
	v_exp_f32_e32 v35, v35
	v_exp_f32_e32 v36, v36
	v_exp_f32_e32 v37, v37
	v_exp_f32_e32 v38, v38
	v_exp_f32_e32 v39, v39
	v_add_f32_e32 v32, 1.0, v32
	v_add_f32_e32 v33, 1.0, v33
	v_add_f32_e32 v34, 1.0, v34
	v_add_f32_e32 v35, 1.0, v35
	v_add_f32_e32 v36, 1.0, v36
	v_add_f32_e32 v37, 1.0, v37
	v_add_f32_e32 v38, 1.0, v38
	v_add_f32_e32 v39, 1.0, v39
	v_rcp_f32_e32 v32, v32
	v_rcp_f32_e32 v33, v33
	v_rcp_f32_e32 v34, v34
	v_rcp_f32_e32 v35, v35
	v_rcp_f32_e32 v36, v36
	v_rcp_f32_e32 v37, v37
	v_rcp_f32_e32 v38, v38
	v_rcp_f32_e32 v39, v39
	s_nop 0
	v_pk_mul_f32 v[136:137], v[136:137], v[32:33]
	v_pk_mul_f32 v[138:139], v[138:139], v[34:35]
	v_pk_mul_f32 v[152:153], v[152:153], v[36:37]
	v_pk_mul_f32 v[154:155], v[154:155], v[38:39]
	v_cvt_pk_bf16_f32 v64, v136, v137
	v_cvt_pk_bf16_f32 v65, v138, v139
	v_cvt_pk_bf16_f32 v66, v152, v153
	v_cvt_pk_bf16_f32 v67, v154, v155
	global_store_dwordx2 v18, v[64:65], s[10:11]
	global_store_dwordx2 v18, v[66:67], s[10:11] offset:32
	v_pk_mul_f32 v[168:169], v[168:169], v[24:25] op_sel_hi:[1,0]
	v_pk_mul_f32 v[170:171], v[170:171], v[24:25] op_sel_hi:[1,0]
	v_pk_mul_f32 v[184:185], v[184:185], v[24:25] op_sel_hi:[1,0]
	v_pk_mul_f32 v[186:187], v[186:187], v[24:25] op_sel_hi:[1,0]
	v_mul_f32_e32 v48, 0x3dd2d3e8, v168
	v_mul_f32_e32 v49, 0x3dd2d3e8, v169
	v_mul_f32_e32 v50, 0x3dd2d3e8, v170
	v_mul_f32_e32 v51, 0x3dd2d3e8, v171
	v_mul_f32_e32 v52, 0x3dd2d3e8, v184
	v_mul_f32_e32 v53, 0x3dd2d3e8, v185
	v_mul_f32_e32 v54, 0x3dd2d3e8, v186
	v_mul_f32_e32 v55, 0x3dd2d3e8, v187
	v_fma_f32 v48, -v168, v48, s24
	v_fma_f32 v49, -v169, v49, s24
	v_fma_f32 v50, -v170, v50, s24
	v_fma_f32 v51, -v171, v51, s24
	v_fma_f32 v52, -v184, v52, s24
	v_fma_f32 v53, -v185, v53, s24
	v_fma_f32 v54, -v186, v54, s24
	v_fma_f32 v55, -v187, v55, s24
	v_mul_f32_e32 v48, v168, v48
	v_mul_f32_e32 v49, v169, v49
	v_mul_f32_e32 v50, v170, v50
	v_mul_f32_e32 v51, v171, v51
	v_mul_f32_e32 v52, v184, v52
	v_mul_f32_e32 v53, v185, v53
	v_mul_f32_e32 v54, v186, v54
	v_mul_f32_e32 v55, v187, v55
	v_exp_f32_e32 v48, v48
	v_exp_f32_e32 v49, v49
	v_exp_f32_e32 v50, v50
	v_exp_f32_e32 v51, v51
	v_exp_f32_e32 v52, v52
	v_exp_f32_e32 v53, v53
	v_exp_f32_e32 v54, v54
	v_exp_f32_e32 v55, v55
	v_add_f32_e32 v48, 1.0, v48
	v_add_f32_e32 v49, 1.0, v49
	v_add_f32_e32 v50, 1.0, v50
	v_add_f32_e32 v51, 1.0, v51
	v_add_f32_e32 v52, 1.0, v52
	v_add_f32_e32 v53, 1.0, v53
	v_add_f32_e32 v54, 1.0, v54
	v_add_f32_e32 v55, 1.0, v55
	v_rcp_f32_e32 v48, v48
	v_rcp_f32_e32 v49, v49
	v_rcp_f32_e32 v50, v50
	v_rcp_f32_e32 v51, v51
	v_rcp_f32_e32 v52, v52
	v_rcp_f32_e32 v53, v53
	v_rcp_f32_e32 v54, v54
	v_rcp_f32_e32 v55, v55
	s_nop 0
	v_pk_mul_f32 v[168:169], v[168:169], v[48:49]
	v_pk_mul_f32 v[170:171], v[170:171], v[50:51]
	v_pk_mul_f32 v[184:185], v[184:185], v[52:53]
	v_pk_mul_f32 v[186:187], v[186:187], v[54:55]
	v_cvt_pk_bf16_f32 v68, v168, v169
	v_cvt_pk_bf16_f32 v69, v170, v171
	v_cvt_pk_bf16_f32 v70, v184, v185
	v_cvt_pk_bf16_f32 v71, v186, v187
	global_store_dwordx2 v18, v[68:69], s[10:11] offset:64
	global_store_dwordx2 v18, v[70:71], s[10:11] offset:96
	v_pk_mul_f32 v[200:201], v[200:201], v[24:25] op_sel_hi:[1,0]
	v_pk_mul_f32 v[202:203], v[202:203], v[24:25] op_sel_hi:[1,0]
	v_pk_mul_f32 v[216:217], v[216:217], v[24:25] op_sel_hi:[1,0]
	v_pk_mul_f32 v[218:219], v[218:219], v[24:25] op_sel_hi:[1,0]
	v_mul_f32_e32 v32, 0x3dd2d3e8, v200
	v_mul_f32_e32 v33, 0x3dd2d3e8, v201
	v_mul_f32_e32 v34, 0x3dd2d3e8, v202
	v_mul_f32_e32 v35, 0x3dd2d3e8, v203
	v_mul_f32_e32 v36, 0x3dd2d3e8, v216
	v_mul_f32_e32 v37, 0x3dd2d3e8, v217
	v_mul_f32_e32 v38, 0x3dd2d3e8, v218
	v_mul_f32_e32 v39, 0x3dd2d3e8, v219
	v_fma_f32 v32, -v200, v32, s24
	v_fma_f32 v33, -v201, v33, s24
	v_fma_f32 v34, -v202, v34, s24
	v_fma_f32 v35, -v203, v35, s24
	v_fma_f32 v36, -v216, v36, s24
	v_fma_f32 v37, -v217, v37, s24
	v_fma_f32 v38, -v218, v38, s24
	v_fma_f32 v39, -v219, v39, s24
	v_mul_f32_e32 v32, v200, v32
	v_mul_f32_e32 v33, v201, v33
	v_mul_f32_e32 v34, v202, v34
	v_mul_f32_e32 v35, v203, v35
	v_mul_f32_e32 v36, v216, v36
	v_mul_f32_e32 v37, v217, v37
	v_mul_f32_e32 v38, v218, v38
	v_mul_f32_e32 v39, v219, v39
	v_exp_f32_e32 v32, v32
	v_exp_f32_e32 v33, v33
	v_exp_f32_e32 v34, v34
	v_exp_f32_e32 v35, v35
	v_exp_f32_e32 v36, v36
	v_exp_f32_e32 v37, v37
	v_exp_f32_e32 v38, v38
	v_exp_f32_e32 v39, v39
	v_add_f32_e32 v32, 1.0, v32
	v_add_f32_e32 v33, 1.0, v33
	v_add_f32_e32 v34, 1.0, v34
	v_add_f32_e32 v35, 1.0, v35
	v_add_f32_e32 v36, 1.0, v36
	v_add_f32_e32 v37, 1.0, v37
	v_add_f32_e32 v38, 1.0, v38
	v_add_f32_e32 v39, 1.0, v39
	v_rcp_f32_e32 v32, v32
	v_rcp_f32_e32 v33, v33
	v_rcp_f32_e32 v34, v34
	v_rcp_f32_e32 v35, v35
	v_rcp_f32_e32 v36, v36
	v_rcp_f32_e32 v37, v37
	v_rcp_f32_e32 v38, v38
	v_rcp_f32_e32 v39, v39
	s_nop 0
	v_pk_mul_f32 v[200:201], v[200:201], v[32:33]
	v_pk_mul_f32 v[202:203], v[202:203], v[34:35]
	v_pk_mul_f32 v[216:217], v[216:217], v[36:37]
	v_pk_mul_f32 v[218:219], v[218:219], v[38:39]
	v_cvt_pk_bf16_f32 v64, v200, v201
	v_cvt_pk_bf16_f32 v65, v202, v203
	v_cvt_pk_bf16_f32 v66, v216, v217
	v_cvt_pk_bf16_f32 v67, v218, v219
	global_store_dwordx2 v18, v[64:65], s[10:11] offset:128
	global_store_dwordx2 v18, v[66:67], s[10:11] offset:160
	v_pk_mul_f32 v[232:233], v[232:233], v[24:25] op_sel_hi:[1,0]
	v_pk_mul_f32 v[234:235], v[234:235], v[24:25] op_sel_hi:[1,0]
	v_pk_mul_f32 v[248:249], v[248:249], v[24:25] op_sel_hi:[1,0]
	v_pk_mul_f32 v[250:251], v[250:251], v[24:25] op_sel_hi:[1,0]
	v_mul_f32_e32 v48, 0x3dd2d3e8, v232
	v_mul_f32_e32 v49, 0x3dd2d3e8, v233
	v_mul_f32_e32 v50, 0x3dd2d3e8, v234
	v_mul_f32_e32 v51, 0x3dd2d3e8, v235
	v_mul_f32_e32 v52, 0x3dd2d3e8, v248
	v_mul_f32_e32 v53, 0x3dd2d3e8, v249
	v_mul_f32_e32 v54, 0x3dd2d3e8, v250
	v_mul_f32_e32 v55, 0x3dd2d3e8, v251
	v_fma_f32 v48, -v232, v48, s24
	v_fma_f32 v49, -v233, v49, s24
	v_fma_f32 v50, -v234, v50, s24
	v_fma_f32 v51, -v235, v51, s24
	v_fma_f32 v52, -v248, v52, s24
	v_fma_f32 v53, -v249, v53, s24
	v_fma_f32 v54, -v250, v54, s24
	v_fma_f32 v55, -v251, v55, s24
	v_mul_f32_e32 v48, v232, v48
	v_mul_f32_e32 v49, v233, v49
	v_mul_f32_e32 v50, v234, v50
	v_mul_f32_e32 v51, v235, v51
	v_mul_f32_e32 v52, v248, v52
	v_mul_f32_e32 v53, v249, v53
	v_mul_f32_e32 v54, v250, v54
	v_mul_f32_e32 v55, v251, v55
	v_exp_f32_e32 v48, v48
	v_exp_f32_e32 v49, v49
	v_exp_f32_e32 v50, v50
	v_exp_f32_e32 v51, v51
	v_exp_f32_e32 v52, v52
	v_exp_f32_e32 v53, v53
	v_exp_f32_e32 v54, v54
	v_exp_f32_e32 v55, v55
	v_add_f32_e32 v48, 1.0, v48
	v_add_f32_e32 v49, 1.0, v49
	v_add_f32_e32 v50, 1.0, v50
	v_add_f32_e32 v51, 1.0, v51
	v_add_f32_e32 v52, 1.0, v52
	v_add_f32_e32 v53, 1.0, v53
	v_add_f32_e32 v54, 1.0, v54
	v_add_f32_e32 v55, 1.0, v55
	v_rcp_f32_e32 v48, v48
	v_rcp_f32_e32 v49, v49
	v_rcp_f32_e32 v50, v50
	v_rcp_f32_e32 v51, v51
	v_rcp_f32_e32 v52, v52
	v_rcp_f32_e32 v53, v53
	v_rcp_f32_e32 v54, v54
	v_rcp_f32_e32 v55, v55
	s_nop 0
	v_pk_mul_f32 v[232:233], v[232:233], v[48:49]
	v_pk_mul_f32 v[234:235], v[234:235], v[50:51]
	v_pk_mul_f32 v[248:249], v[248:249], v[52:53]
	v_pk_mul_f32 v[250:251], v[250:251], v[54:55]
	v_cvt_pk_bf16_f32 v68, v232, v233
	v_cvt_pk_bf16_f32 v69, v234, v235
	v_cvt_pk_bf16_f32 v70, v248, v249
	v_cvt_pk_bf16_f32 v71, v250, v251
	global_store_dwordx2 v18, v[68:69], s[10:11] offset:192
	global_store_dwordx2 v18, v[70:71], s[10:11] offset:224
	v_pk_mul_f32 v[140:141], v[140:141], v[26:27] op_sel_hi:[1,0]
	v_pk_mul_f32 v[142:143], v[142:143], v[26:27] op_sel_hi:[1,0]
	v_pk_mul_f32 v[156:157], v[156:157], v[26:27] op_sel_hi:[1,0]
	v_pk_mul_f32 v[158:159], v[158:159], v[26:27] op_sel_hi:[1,0]
	v_mul_f32_e32 v32, 0x3dd2d3e8, v140
	v_mul_f32_e32 v33, 0x3dd2d3e8, v141
	v_mul_f32_e32 v34, 0x3dd2d3e8, v142
	v_mul_f32_e32 v35, 0x3dd2d3e8, v143
	v_mul_f32_e32 v36, 0x3dd2d3e8, v156
	v_mul_f32_e32 v37, 0x3dd2d3e8, v157
	v_mul_f32_e32 v38, 0x3dd2d3e8, v158
	v_mul_f32_e32 v39, 0x3dd2d3e8, v159
	v_fma_f32 v32, -v140, v32, s24
	v_fma_f32 v33, -v141, v33, s24
	v_fma_f32 v34, -v142, v34, s24
	v_fma_f32 v35, -v143, v35, s24
	v_fma_f32 v36, -v156, v36, s24
	v_fma_f32 v37, -v157, v37, s24
	v_fma_f32 v38, -v158, v38, s24
	v_fma_f32 v39, -v159, v39, s24
	v_mul_f32_e32 v32, v140, v32
	v_mul_f32_e32 v33, v141, v33
	v_mul_f32_e32 v34, v142, v34
	v_mul_f32_e32 v35, v143, v35
	v_mul_f32_e32 v36, v156, v36
	v_mul_f32_e32 v37, v157, v37
	v_mul_f32_e32 v38, v158, v38
	v_mul_f32_e32 v39, v159, v39
	v_exp_f32_e32 v32, v32
	v_exp_f32_e32 v33, v33
	v_exp_f32_e32 v34, v34
	v_exp_f32_e32 v35, v35
	v_exp_f32_e32 v36, v36
	v_exp_f32_e32 v37, v37
	v_exp_f32_e32 v38, v38
	v_exp_f32_e32 v39, v39
	v_add_f32_e32 v32, 1.0, v32
	v_add_f32_e32 v33, 1.0, v33
	v_add_f32_e32 v34, 1.0, v34
	v_add_f32_e32 v35, 1.0, v35
	v_add_f32_e32 v36, 1.0, v36
	v_add_f32_e32 v37, 1.0, v37
	v_add_f32_e32 v38, 1.0, v38
	v_add_f32_e32 v39, 1.0, v39
	v_rcp_f32_e32 v32, v32
	v_rcp_f32_e32 v33, v33
	v_rcp_f32_e32 v34, v34
	v_rcp_f32_e32 v35, v35
	v_rcp_f32_e32 v36, v36
	v_rcp_f32_e32 v37, v37
	v_rcp_f32_e32 v38, v38
	v_rcp_f32_e32 v39, v39
	s_nop 0
	v_pk_mul_f32 v[140:141], v[140:141], v[32:33]
	v_pk_mul_f32 v[142:143], v[142:143], v[34:35]
	v_pk_mul_f32 v[156:157], v[156:157], v[36:37]
	v_pk_mul_f32 v[158:159], v[158:159], v[38:39]
	v_cvt_pk_bf16_f32 v64, v140, v141
	v_cvt_pk_bf16_f32 v65, v142, v143
	v_cvt_pk_bf16_f32 v66, v156, v157
	v_cvt_pk_bf16_f32 v67, v158, v159
	global_store_dwordx2 v19, v[64:65], s[10:11]
	global_store_dwordx2 v19, v[66:67], s[10:11] offset:32
	v_pk_mul_f32 v[172:173], v[172:173], v[26:27] op_sel_hi:[1,0]
	v_pk_mul_f32 v[174:175], v[174:175], v[26:27] op_sel_hi:[1,0]
	v_pk_mul_f32 v[188:189], v[188:189], v[26:27] op_sel_hi:[1,0]
	v_pk_mul_f32 v[190:191], v[190:191], v[26:27] op_sel_hi:[1,0]
	v_mul_f32_e32 v48, 0x3dd2d3e8, v172
	v_mul_f32_e32 v49, 0x3dd2d3e8, v173
	v_mul_f32_e32 v50, 0x3dd2d3e8, v174
	v_mul_f32_e32 v51, 0x3dd2d3e8, v175
	v_mul_f32_e32 v52, 0x3dd2d3e8, v188
	v_mul_f32_e32 v53, 0x3dd2d3e8, v189
	v_mul_f32_e32 v54, 0x3dd2d3e8, v190
	v_mul_f32_e32 v55, 0x3dd2d3e8, v191
	v_fma_f32 v48, -v172, v48, s24
	v_fma_f32 v49, -v173, v49, s24
	v_fma_f32 v50, -v174, v50, s24
	v_fma_f32 v51, -v175, v51, s24
	v_fma_f32 v52, -v188, v52, s24
	v_fma_f32 v53, -v189, v53, s24
	v_fma_f32 v54, -v190, v54, s24
	v_fma_f32 v55, -v191, v55, s24
	v_mul_f32_e32 v48, v172, v48
	v_mul_f32_e32 v49, v173, v49
	v_mul_f32_e32 v50, v174, v50
	v_mul_f32_e32 v51, v175, v51
	v_mul_f32_e32 v52, v188, v52
	v_mul_f32_e32 v53, v189, v53
	v_mul_f32_e32 v54, v190, v54
	v_mul_f32_e32 v55, v191, v55
	v_exp_f32_e32 v48, v48
	v_exp_f32_e32 v49, v49
	v_exp_f32_e32 v50, v50
	v_exp_f32_e32 v51, v51
	v_exp_f32_e32 v52, v52
	v_exp_f32_e32 v53, v53
	v_exp_f32_e32 v54, v54
	v_exp_f32_e32 v55, v55
	v_add_f32_e32 v48, 1.0, v48
	v_add_f32_e32 v49, 1.0, v49
	v_add_f32_e32 v50, 1.0, v50
	v_add_f32_e32 v51, 1.0, v51
	v_add_f32_e32 v52, 1.0, v52
	v_add_f32_e32 v53, 1.0, v53
	v_add_f32_e32 v54, 1.0, v54
	v_add_f32_e32 v55, 1.0, v55
	v_rcp_f32_e32 v48, v48
	v_rcp_f32_e32 v49, v49
	v_rcp_f32_e32 v50, v50
	v_rcp_f32_e32 v51, v51
	v_rcp_f32_e32 v52, v52
	v_rcp_f32_e32 v53, v53
	v_rcp_f32_e32 v54, v54
	v_rcp_f32_e32 v55, v55
	s_nop 0
	v_pk_mul_f32 v[172:173], v[172:173], v[48:49]
	v_pk_mul_f32 v[174:175], v[174:175], v[50:51]
	v_pk_mul_f32 v[188:189], v[188:189], v[52:53]
	v_pk_mul_f32 v[190:191], v[190:191], v[54:55]
	v_cvt_pk_bf16_f32 v68, v172, v173
	v_cvt_pk_bf16_f32 v69, v174, v175
	v_cvt_pk_bf16_f32 v70, v188, v189
	v_cvt_pk_bf16_f32 v71, v190, v191
	global_store_dwordx2 v19, v[68:69], s[10:11] offset:64
	global_store_dwordx2 v19, v[70:71], s[10:11] offset:96
	v_pk_mul_f32 v[204:205], v[204:205], v[26:27] op_sel_hi:[1,0]
	v_pk_mul_f32 v[206:207], v[206:207], v[26:27] op_sel_hi:[1,0]
	v_pk_mul_f32 v[220:221], v[220:221], v[26:27] op_sel_hi:[1,0]
	v_pk_mul_f32 v[222:223], v[222:223], v[26:27] op_sel_hi:[1,0]
	v_mul_f32_e32 v32, 0x3dd2d3e8, v204
	v_mul_f32_e32 v33, 0x3dd2d3e8, v205
	v_mul_f32_e32 v34, 0x3dd2d3e8, v206
	v_mul_f32_e32 v35, 0x3dd2d3e8, v207
	v_mul_f32_e32 v36, 0x3dd2d3e8, v220
	v_mul_f32_e32 v37, 0x3dd2d3e8, v221
	v_mul_f32_e32 v38, 0x3dd2d3e8, v222
	v_mul_f32_e32 v39, 0x3dd2d3e8, v223
	v_fma_f32 v32, -v204, v32, s24
	v_fma_f32 v33, -v205, v33, s24
	v_fma_f32 v34, -v206, v34, s24
	v_fma_f32 v35, -v207, v35, s24
	v_fma_f32 v36, -v220, v36, s24
	v_fma_f32 v37, -v221, v37, s24
	v_fma_f32 v38, -v222, v38, s24
	v_fma_f32 v39, -v223, v39, s24
	v_mul_f32_e32 v32, v204, v32
	v_mul_f32_e32 v33, v205, v33
	v_mul_f32_e32 v34, v206, v34
	v_mul_f32_e32 v35, v207, v35
	v_mul_f32_e32 v36, v220, v36
	v_mul_f32_e32 v37, v221, v37
	v_mul_f32_e32 v38, v222, v38
	v_mul_f32_e32 v39, v223, v39
	v_exp_f32_e32 v32, v32
	v_exp_f32_e32 v33, v33
	v_exp_f32_e32 v34, v34
	v_exp_f32_e32 v35, v35
	v_exp_f32_e32 v36, v36
	v_exp_f32_e32 v37, v37
	v_exp_f32_e32 v38, v38
	v_exp_f32_e32 v39, v39
	v_add_f32_e32 v32, 1.0, v32
	v_add_f32_e32 v33, 1.0, v33
	v_add_f32_e32 v34, 1.0, v34
	v_add_f32_e32 v35, 1.0, v35
	v_add_f32_e32 v36, 1.0, v36
	v_add_f32_e32 v37, 1.0, v37
	v_add_f32_e32 v38, 1.0, v38
	v_add_f32_e32 v39, 1.0, v39
	v_rcp_f32_e32 v32, v32
	v_rcp_f32_e32 v33, v33
	v_rcp_f32_e32 v34, v34
	v_rcp_f32_e32 v35, v35
	v_rcp_f32_e32 v36, v36
	v_rcp_f32_e32 v37, v37
	v_rcp_f32_e32 v38, v38
	v_rcp_f32_e32 v39, v39
	s_nop 0
	v_pk_mul_f32 v[204:205], v[204:205], v[32:33]
	v_pk_mul_f32 v[206:207], v[206:207], v[34:35]
	v_pk_mul_f32 v[220:221], v[220:221], v[36:37]
	v_pk_mul_f32 v[222:223], v[222:223], v[38:39]
	v_cvt_pk_bf16_f32 v64, v204, v205
	v_cvt_pk_bf16_f32 v65, v206, v207
	v_cvt_pk_bf16_f32 v66, v220, v221
	v_cvt_pk_bf16_f32 v67, v222, v223
	global_store_dwordx2 v19, v[64:65], s[10:11] offset:128
	global_store_dwordx2 v19, v[66:67], s[10:11] offset:160
	v_pk_mul_f32 v[236:237], v[236:237], v[26:27] op_sel_hi:[1,0]
	v_pk_mul_f32 v[238:239], v[238:239], v[26:27] op_sel_hi:[1,0]
	v_pk_mul_f32 v[252:253], v[252:253], v[26:27] op_sel_hi:[1,0]
	v_pk_mul_f32 v[254:255], v[254:255], v[26:27] op_sel_hi:[1,0]
	v_mul_f32_e32 v48, 0x3dd2d3e8, v236
	v_mul_f32_e32 v49, 0x3dd2d3e8, v237
	v_mul_f32_e32 v50, 0x3dd2d3e8, v238
	v_mul_f32_e32 v51, 0x3dd2d3e8, v239
	v_mul_f32_e32 v52, 0x3dd2d3e8, v252
	v_mul_f32_e32 v53, 0x3dd2d3e8, v253
	v_mul_f32_e32 v54, 0x3dd2d3e8, v254
	v_mul_f32_e32 v55, 0x3dd2d3e8, v255
	v_fma_f32 v48, -v236, v48, s24
	v_fma_f32 v49, -v237, v49, s24
	v_fma_f32 v50, -v238, v50, s24
	v_fma_f32 v51, -v239, v51, s24
	v_fma_f32 v52, -v252, v52, s24
	v_fma_f32 v53, -v253, v53, s24
	v_fma_f32 v54, -v254, v54, s24
	v_fma_f32 v55, -v255, v55, s24
	v_mul_f32_e32 v48, v236, v48
	v_mul_f32_e32 v49, v237, v49
	v_mul_f32_e32 v50, v238, v50
	v_mul_f32_e32 v51, v239, v51
	v_mul_f32_e32 v52, v252, v52
	v_mul_f32_e32 v53, v253, v53
	v_mul_f32_e32 v54, v254, v54
	v_mul_f32_e32 v55, v255, v55
	v_exp_f32_e32 v48, v48
	v_exp_f32_e32 v49, v49
	v_exp_f32_e32 v50, v50
	v_exp_f32_e32 v51, v51
	v_exp_f32_e32 v52, v52
	v_exp_f32_e32 v53, v53
	v_exp_f32_e32 v54, v54
	v_exp_f32_e32 v55, v55
	v_add_f32_e32 v48, 1.0, v48
	v_add_f32_e32 v49, 1.0, v49
	v_add_f32_e32 v50, 1.0, v50
	v_add_f32_e32 v51, 1.0, v51
	v_add_f32_e32 v52, 1.0, v52
	v_add_f32_e32 v53, 1.0, v53
	v_add_f32_e32 v54, 1.0, v54
	v_add_f32_e32 v55, 1.0, v55
	v_rcp_f32_e32 v48, v48
	v_rcp_f32_e32 v49, v49
	v_rcp_f32_e32 v50, v50
	v_rcp_f32_e32 v51, v51
	v_rcp_f32_e32 v52, v52
	v_rcp_f32_e32 v53, v53
	v_rcp_f32_e32 v54, v54
	v_rcp_f32_e32 v55, v55
	s_nop 0
	v_pk_mul_f32 v[236:237], v[236:237], v[48:49]
	v_pk_mul_f32 v[238:239], v[238:239], v[50:51]
	v_pk_mul_f32 v[252:253], v[252:253], v[52:53]
	v_pk_mul_f32 v[254:255], v[254:255], v[54:55]
	v_cvt_pk_bf16_f32 v68, v236, v237
	v_cvt_pk_bf16_f32 v69, v238, v239
	v_cvt_pk_bf16_f32 v70, v252, v253
	v_cvt_pk_bf16_f32 v71, v254, v255
	global_store_dwordx2 v19, v[68:69], s[10:11] offset:192
	global_store_dwordx2 v19, v[70:71], s[10:11] offset:224

	.amdhsa_kernel _Z7gemm128ILi2ELi128EEv8GemmArgs
		.amdhsa_group_segment_fixed_size 81920
		.amdhsa_private_segment_fixed_size 0
		.amdhsa_kernarg_size 80
		.amdhsa_user_sgpr_count 2
		.amdhsa_user_sgpr_dispatch_ptr 0
		.amdhsa_user_sgpr_queue_ptr 0
		.amdhsa_user_sgpr_kernarg_segment_ptr 1
		.amdhsa_user_sgpr_dispatch_id 0
		.amdhsa_user_sgpr_kernarg_preload_length 0
		.amdhsa_user_sgpr_kernarg_preload_offset 0
		.amdhsa_user_sgpr_private_segment_size 0
		.amdhsa_uses_dynamic_stack 0
		.amdhsa_enable_private_segment 0
		.amdhsa_system_sgpr_workgroup_id_x 1
		.amdhsa_system_sgpr_workgroup_id_y 0
		.amdhsa_system_sgpr_workgroup_id_z 0
		.amdhsa_system_sgpr_workgroup_info 0
		.amdhsa_system_vgpr_workitem_id 0
		.amdhsa_next_free_vgpr 256
		.amdhsa_next_free_sgpr 25
		.amdhsa_accum_offset 256
		.amdhsa_reserve_vcc 1
		.amdhsa_float_round_mode_32 0
		.amdhsa_float_round_mode_16_64 0
		.amdhsa_float_denorm_mode_32 3
		.amdhsa_float_denorm_mode_16_64 3
		.amdhsa_dx10_clamp 1
		.amdhsa_ieee_mode 1
		.amdhsa_fp16_overflow 0
		.amdhsa_tg_split 0
		.amdhsa_exception_fp_ieee_invalid_op 0
		.amdhsa_exception_fp_denorm_src 0
		.amdhsa_exception_fp_ieee_div_zero 0
		.amdhsa_exception_fp_ieee_overflow 0
		.amdhsa_exception_fp_ieee_underflow 0
		.amdhsa_exception_fp_ieee_inexact 0
		.amdhsa_exception_int_div_zero 0
	.end_amdhsa_kernel

.Lfunc_end3:
	.size	_Z7gemm128ILi2ELi128EEv8GemmArgs, .Lfunc_end3-_Z7gemm128ILi2ELi128EEv8GemmArgs
	.set _Z7gemm128ILi2ELi128EEv8GemmArgs.num_vgpr, 256
	.set _Z7gemm128ILi2ELi128EEv8GemmArgs.num_agpr, 0
	.set _Z7gemm128ILi2ELi128EEv8GemmArgs.numbered_sgpr, 25
	.set _Z7gemm128ILi2ELi128EEv8GemmArgs.num_named_barrier, 0
	.set _Z7gemm128ILi2ELi128EEv8GemmArgs.private_seg_size, 0
	.set _Z7gemm128ILi2ELi128EEv8GemmArgs.uses_vcc, 1
	.set _Z7gemm128ILi2ELi128EEv8GemmArgs.uses_flat_scratch, 0
	.set _Z7gemm128ILi2ELi128EEv8GemmArgs.has_dyn_sized_stack, 0
	.set _Z7gemm128ILi2ELi128EEv8GemmArgs.has_recursion, 0
	.set _Z7gemm128ILi2ELi128EEv8GemmArgs.has_indirect_call, 0

amdhsa.kernels:
  - .agpr_count:     0
    .args:
      - .offset:         0
        .size:           136
        .value_kind:     by_value
      - .offset:         136
        .size:           4
        .value_kind:     hidden_block_count_x
      - .offset:         140
        .size:           4
        .value_kind:     hidden_block_count_y
      - .offset:         144
        .size:           4
        .value_kind:     hidden_block_count_z
      - .offset:         148
        .size:           2
        .value_kind:     hidden_group_size_x
      - .offset:         150
        .size:           2
        .value_kind:     hidden_group_size_y
      - .offset:         152
        .size:           2
        .value_kind:     hidden_group_size_z
      - .offset:         154
        .size:           2
        .value_kind:     hidden_remainder_x
      - .offset:         156
        .size:           2
        .value_kind:     hidden_remainder_y
      - .offset:         158
        .size:           2
        .value_kind:     hidden_remainder_z
      - .offset:         176
        .size:           8
        .value_kind:     hidden_global_offset_x
      - .offset:         184
        .size:           8
        .value_kind:     hidden_global_offset_y
      - .offset:         192
        .size:           8
        .value_kind:     hidden_global_offset_z
      - .offset:         200
        .size:           2
        .value_kind:     hidden_grid_dims
    .group_segment_fixed_size: 16640
    .kernarg_segment_align: 8
    .kernarg_segment_size: 392
    .language:       OpenCL C
    .language_version:
      - 2
      - 0
    .max_flat_workgroup_size: 256
    .name:           _Z11prep_kernel8PrepArgs
    .private_segment_fixed_size: 0
    .sgpr_count:     26
    .sgpr_spill_count: 0
    .symbol:         _Z11prep_kernel8PrepArgs.kd
    .uniform_work_group_size: 1
    .uses_dynamic_stack: false
    .vgpr_count:     46
    .vgpr_spill_count: 0
    .wavefront_size: 64
  - .agpr_count:     0
    .args:
      - .offset:         0
        .size:           216
        .value_kind:     by_value
    .group_segment_fixed_size: 0
    .kernarg_segment_align: 8
    .kernarg_segment_size: 216
    .language:       OpenCL C
    .language_version:
      - 2
      - 0
    .max_flat_workgroup_size: 512
    .name:           _Z11attn_kernel8AttnArgs
    .private_segment_fixed_size: 0
    .sgpr_count:     82
    .sgpr_spill_count: 0
    .symbol:         _Z11attn_kernel8AttnArgs.kd
    .uniform_work_group_size: 1
    .uses_dynamic_stack: false
    .vgpr_count:     220
    .vgpr_spill_count: 0
    .wavefront_size: 64
  - .agpr_count:     0
    .args:
      - .offset:         0
        .size:           80
        .value_kind:     by_value
    .group_segment_fixed_size: 98304
    .kernarg_segment_align: 8
    .kernarg_segment_size: 80
    .language:       OpenCL C
    .language_version:
      - 2
      - 0
    .max_flat_workgroup_size: 256
    .name:           _Z7gemm128ILi1ELi96EEv8GemmArgs
    .private_segment_fixed_size: 0
    .sgpr_count:     37
    .sgpr_spill_count: 0
    .symbol:         _Z7gemm128ILi1ELi96EEv8GemmArgs.kd
    .uniform_work_group_size: 1
    .uses_dynamic_stack: false
    .vgpr_count:     256
    .vgpr_spill_count: 0
    .wavefront_size: 64
  - .agpr_count:     0
    .args:
      - .offset:         0
        .size:           80
        .value_kind:     by_value
    .group_segment_fixed_size: 81920
    .kernarg_segment_align: 8
    .kernarg_segment_size: 80
    .language:       OpenCL C
    .language_version:
      - 2
      - 0
    .max_flat_workgroup_size: 256
    .name:           _Z7gemm128ILi2ELi128EEv8GemmArgs
    .private_segment_fixed_size: 0
    .sgpr_count:     31
    .sgpr_spill_count: 0
    .symbol:         _Z7gemm128ILi2ELi128EEv8GemmArgs.kd
    .uniform_work_group_size: 1
    .uses_dynamic_stack: false
    .vgpr_count:     256
    .vgpr_spill_count: 0
    .wavefront_size: 64
  - .agpr_count:     0
    .args:
      - .offset:         0
        .size:           80
        .value_kind:     by_value
    .group_segment_fixed_size: 98304
    .kernarg_segment_align: 8
    .kernarg_segment_size: 80
    .language:       OpenCL C
    .language_version:
      - 2
      - 0
    .max_flat_workgroup_size: 256
    .name:           _Z7gemm128ILi3ELi96EEv8GemmArgs
    .private_segment_fixed_size: 0
    .sgpr_count:     30
    .sgpr_spill_count: 0
    .symbol:         _Z7gemm128ILi3ELi96EEv8GemmArgs.kd
    .uniform_work_group_size: 1
    .uses_dynamic_stack: false
    .vgpr_count:     256
    .vgpr_spill_count: 0
    .wavefront_size: 64
  - .agpr_count:     0
    .args:
      - .offset:         0
        .size:           32
        .value_kind:     by_value
      - .offset:         32
        .size:           56
        .value_kind:     by_value
    .group_segment_fixed_size: 0
    .kernarg_segment_align: 8
    .kernarg_segment_size: 88
    .language:       OpenCL C
    .language_version:
      - 2
      - 0
    .max_flat_workgroup_size: 512
    .name:           _Z8gemm_bigIN3pg86EpiQKVEEvNS0_4GemmET_
    .private_segment_fixed_size: 0
    .sgpr_count:     58
    .sgpr_spill_count: 0
    .symbol:         _Z8gemm_bigIN3pg86EpiQKVEEvNS0_4GemmET_.kd
    .uniform_work_group_size: 1
    .uses_dynamic_stack: false
    .vgpr_count:     228
    .vgpr_spill_count: 0
    .wavefront_size: 64
  - .agpr_count:     0
    .args:
      - .offset:         0
        .size:           32
        .value_kind:     by_value
      - .offset:         32
        .size:           32
        .value_kind:     by_value
    .group_segment_fixed_size: 0
    .kernarg_segment_align: 8
    .kernarg_segment_size: 64
    .language:       OpenCL C
    .language_version:
      - 2
      - 0
    .max_flat_workgroup_size: 512
    .name:           _Z8gemm_bigIN3pg85EpiUPEEvNS0_4GemmET_
    .private_segment_fixed_size: 0
    .sgpr_count:     50
    .sgpr_spill_count: 0
    .symbol:         _Z8gemm_bigIN3pg85EpiUPEEvNS0_4GemmET_.kd
    .uniform_work_group_size: 1
    .uses_dynamic_stack: false
    .vgpr_count:     226
    .vgpr_spill_count: 0
    .wavefront_size: 64
